# attn_fast: waves 4-7 skip the duplicated S/N1/softmax phase, run only the address-mask-load slice and get its 21 result registers through LDS
# speedup vs baseline: 1.0105x; 1.0105x over previous
_Z9attn_fastPKtS0_S0_S0_S0_S0_S0_S0_S0_PKfS2_Pt:
	s_load_dwordx8 s[36:43], s[0:1], 0x40
	v_and_b32_e32 v152, 63, v0
	v_bfe_u32 v153, v0, 6, 2
	v_mul_u32_u24_e32 v153, 0x1800, v153
	v_lshl_add_u32 v154, v152, 2, v153
	v_lshl_add_u32 v155, v152, 3, v153
	v_lshl_add_u32 v152, v152, 4, v153
	v_mov_b32_e32 v153, v155
	s_load_dwordx8 s[24:31], s[0:1], 0x0
	s_load_dwordx8 s[4:11], s[0:1], 0x20
	v_lshrrev_b32_e32 v2, 5, v0
	s_ashr_i32 s3, s2, 31
	v_bitop3_b32 v3, v2, v0, 31 bitop3:0x78
	v_lshlrev_b32_e32 v3, 4, v3
	v_lshlrev_b32_e32 v70, 4, v0
	s_lshl_b64 s[34:35], s[2:3], 15
	v_lshlrev_b32_e32 v2, 9, v2
	v_or_b32_e32 v6, 0xfffffe00, v0
	v_add_u32_e32 v7, 0, v70
	v_or3_b32 v2, s34, v2, v3
	v_mov_b32_e32 v3, s35
	v_mov_b32_e32 v1, v0
	v_add_u32_e32 v8, 0x18000, v7
	s_waitcnt lgkmcnt(0)
	v_lshl_add_u64 v[4:5], s[24:25], 0, v[2:3]
	s_mov_b64 s[0:1], 0
	s_mov_b64 s[12:13], 0x2000
	s_movk_i32 s14, 0x5ff
	v_mov_b32_e32 v9, v6

.LBB12_15:
	v_add_u32_e32 v79, s33, v70
	v_bitop3_b32 v68, v70, s6, v1 bitop3:0x48
	v_readfirstlane_b32 s8, v79
	v_lshl_add_u64 v[80:81], v[66:67], 0, v[68:69]
	s_mov_b32 m0, s8
	v_add_u32_e32 v68, 0x200, v1
	global_load_lds_dwordx4 v[80:81], off
	v_cmp_lt_u32_e32 vcc, s7, v1
	v_add_u32_e32 v70, 0x2000, v70
	v_lshl_add_u64 v[66:67], v[66:67], 0, s[4:5]
	s_or_b64 s[0:1], vcc, s[0:1]
	v_mov_b32_e32 v1, v68
	s_andn2_b64 exec, exec, s[0:1]
	s_cbranch_execnz .LBB12_15
	s_or_b64 exec, exec, s[0:1]
	v_readfirstlane_b32 s44, v0
	s_nop 3
	s_cmp_lt_u32 s44, 0x100
	s_cbranch_scc0 .Lat_dh1
	v_lshl_add_u32 v1, v103, 9, 0
	v_add_u32_e32 v114, v1, v78
	v_add_u32_e32 v117, v1, v77
	ds_read_b128 v[66:69], v114
	ds_read_b128 v[78:81], v114 offset:8192
	ds_read_b128 v[82:85], v117
	ds_read_b128 v[86:89], v117 offset:8192
	s_waitcnt lgkmcnt(0)
	v_mfma_f32_16x16x32_bf16 v[66:69], v[66:69], v[62:65], 0
	v_add_u32_e32 v115, v1, v76
	v_add_u32_e32 v113, v1, v75
	v_add_u32_e32 v119, v1, v74
	v_mfma_f32_16x16x32_bf16 v[78:81], v[78:81], v[62:65], 0
	v_add_u32_e32 v118, v1, v72
	v_add_u32_e32 v116, v1, v73
	v_add_u32_e32 v1, v1, v71
	v_mfma_f32_16x16x32_bf16 v[66:69], v[82:85], v[58:61], v[66:69]
	s_mov_b32 s38, 0x5040100
	s_add_u32 s36, s30, s34
	s_addc_u32 s37, s31, s35
	v_mfma_f32_16x16x32_bf16 v[76:79], v[86:89], v[58:61], v[78:81]
	ds_read_b128 v[84:87], v115 offset:8192
	ds_read_b128 v[88:91], v113 offset:8192
	s_add_i32 s30, 0, 0x20000
	ds_read_b128 v[80:83], v115
	s_waitcnt lgkmcnt(0)
	v_mfma_f32_16x16x32_bf16 v[66:69], v[80:83], v[54:57], v[66:69]
	ds_read_b128 v[80:83], v113
	ds_read_b128 v[92:95], v119 offset:8192
	v_lshlrev_b32_e32 v112, 7, v103
	s_waitcnt lgkmcnt(0)
	v_mfma_f32_16x16x32_bf16 v[66:69], v[80:83], v[50:53], v[66:69]
	ds_read_b128 v[80:83], v119
	ds_read_b128 v[72:75], v118 offset:8192
	s_add_i32 s34, 0, 0x22000
	s_waitcnt lgkmcnt(0)
	v_mfma_f32_16x16x32_bf16 v[66:69], v[80:83], v[46:49], v[66:69]
	ds_read_b128 v[80:83], v118
	ds_read_b128 v[96:99], v116 offset:8192
	s_waitcnt lgkmcnt(0)
	v_mfma_f32_16x16x32_bf16 v[66:69], v[80:83], v[42:45], v[66:69]
	ds_read_b128 v[80:83], v116
	v_mfma_f32_16x16x32_bf16 v[76:79], v[84:87], v[54:57], v[76:79]
	v_mfma_f32_16x16x32_bf16 v[76:79], v[88:91], v[50:53], v[76:79]
	s_waitcnt lgkmcnt(0)
	v_mfma_f32_16x16x32_bf16 v[66:69], v[80:83], v[38:41], v[66:69]
	ds_read_b128 v[80:83], v1
	ds_read_b128 v[106:109], v1 offset:8192
	v_mfma_f32_16x16x32_bf16 v[76:79], v[92:95], v[46:49], v[76:79]
	s_waitcnt lgkmcnt(0)
	v_mfma_f32_16x16x32_bf16 v[66:69], v[80:83], v[34:37], v[66:69]
	v_mfma_f32_16x16x32_bf16 v[70:73], v[72:75], v[42:45], v[76:79]
	s_nop 4
	ds_read_b128 v[74:77], v114 offset:16384
	ds_read_b128 v[78:81], v114 offset:24576
	ds_read_b128 v[82:85], v117 offset:16384
	ds_read_b128 v[86:89], v117 offset:24576
	s_waitcnt lgkmcnt(0)
	v_mfma_f32_16x16x32_bf16 v[74:77], v[74:77], v[62:65], 0
	v_mfma_f32_16x16x32_bf16 v[74:77], v[82:85], v[58:61], v[74:77]
	ds_read_b128 v[82:85], v115 offset:16384
	ds_read_b128 v[90:93], v115 offset:24576
	v_mfma_f32_16x16x32_bf16 v[70:73], v[96:99], v[38:41], v[70:73]
	s_waitcnt lgkmcnt(0)
	v_mfma_f32_16x16x32_bf16 v[74:77], v[82:85], v[54:57], v[74:77]
	ds_read_b128 v[82:85], v113 offset:16384
	ds_read_b128 v[94:97], v113 offset:24576
	v_mfma_f32_16x16x32_bf16 v[78:81], v[78:81], v[62:65], 0
	s_waitcnt lgkmcnt(0)
	v_mfma_f32_16x16x32_bf16 v[74:77], v[82:85], v[50:53], v[74:77]
	ds_read_b128 v[82:85], v119 offset:16384
	ds_read_b128 v[98:101], v119 offset:24576
	v_mfma_f32_16x16x32_bf16 v[78:81], v[86:89], v[58:61], v[78:81]
	v_mfma_f32_16x16x32_bf16 v[70:73], v[106:109], v[34:37], v[70:73]
	s_waitcnt lgkmcnt(0)
	v_mfma_f32_16x16x32_bf16 v[74:77], v[82:85], v[46:49], v[74:77]
	ds_read_b128 v[82:85], v118 offset:16384
	ds_read_b128 v[106:109], v118 offset:24576
	s_nop 3
	v_cvt_pk_bf16_f32 v70, v70, s0
	v_cvt_pk_bf16_f32 v71, v71, s0
	v_mfma_f32_16x16x32_bf16 v[78:81], v[90:93], v[54:57], v[78:81]
	v_cvt_pk_bf16_f32 v72, v72, s0
	v_cvt_pk_bf16_f32 v73, v73, s0
	s_waitcnt lgkmcnt(0)
	v_mfma_f32_16x16x32_bf16 v[74:77], v[82:85], v[42:45], v[74:77]
	ds_read_b128 v[82:85], v116 offset:16384
	ds_read_b128 v[120:123], v116 offset:24576
	v_mfma_f32_16x16x32_bf16 v[78:81], v[94:97], v[50:53], v[78:81]
	s_waitcnt lgkmcnt(0)
	v_mfma_f32_16x16x32_bf16 v[74:77], v[82:85], v[38:41], v[74:77]
	ds_read_b128 v[82:85], v1 offset:16384
	ds_read_b128 v[124:127], v1 offset:24576
	v_mfma_f32_16x16x32_bf16 v[78:81], v[98:101], v[46:49], v[78:81]
	s_waitcnt lgkmcnt(0)
	v_mfma_f32_16x16x32_bf16 v[74:77], v[82:85], v[34:37], v[74:77]
	v_cvt_pk_bf16_f32 v82, v66, s0
	v_cvt_pk_bf16_f32 v83, v67, s0
	v_cvt_pk_bf16_f32 v84, v68, s0
	v_cvt_pk_bf16_f32 v85, v69, s0
	v_mfma_f32_16x16x32_bf16 v[66:69], v[106:109], v[42:45], v[78:81]
	v_lshlrev_b32_e32 v106, 2, v104
	v_cmp_gt_u32_e32 vcc, v106, v102
	v_mfma_f32_16x16x32_bf16 v[66:69], v[120:123], v[38:41], v[66:69]
	v_cvt_pk_bf16_f32 v78, v74, s0
	v_or_b32_e32 v74, 3, v106
	v_cvt_pk_bf16_f32 v79, v75, s0
	v_mfma_f32_16x16x32_bf16 v[66:69], v[124:127], v[34:37], v[66:69]
	v_cvt_pk_bf16_f32 v80, v76, s0
	v_cvt_pk_bf16_f32 v81, v77, s0
	v_cmp_gt_u32_e64 s[6:7], v74, v102
	v_cndmask_b32_e64 v75, v82, 0, vcc
	v_or_b32_e32 v120, 51, v106
	s_nop 2
	v_cvt_pk_bf16_f32 v89, v69, s0
	v_or_b32_e32 v69, 2, v106
	v_cvt_pk_bf16_f32 v66, v66, s0
	v_cvt_pk_bf16_f32 v67, v67, s0
	v_cvt_pk_bf16_f32 v68, v68, s0
	v_cmp_lt_u32_e64 s[0:1], v106, v102
	v_cmp_gt_u32_e64 s[4:5], v69, v102
	v_cndmask_b32_e64 v77, v85, 0, s[6:7]
	v_cndmask_b32_e64 v76, 0, v83, s[0:1]
	v_cndmask_b32_e64 v69, v84, 0, s[4:5]
	v_perm_b32 v74, v76, v75, s38
	v_perm_b32 v75, v77, v69, s38
	v_or_b32_e32 v69, 17, v106
	v_or_b32_e32 v76, 16, v106
	v_cmp_gt_u32_e64 s[8:9], v76, v102
	v_cmp_gt_u32_e64 s[10:11], v69, v102
	s_nop 0
	v_cndmask_b32_e64 v70, v70, 0, s[8:9]
	v_cndmask_b32_e64 v69, v71, 0, s[10:11]
	v_perm_b32 v76, v69, v70, s38
	v_or_b32_e32 v69, 19, v106
	v_or_b32_e32 v70, 18, v106
	v_cmp_gt_u32_e64 s[16:17], v70, v102
	v_cmp_gt_u32_e64 s[20:21], v69, v102
	v_or_b32_e32 v71, 35, v106
	v_cndmask_b32_e64 v70, v72, 0, s[16:17]
	v_cndmask_b32_e64 v69, v73, 0, s[20:21]
	v_perm_b32 v77, v69, v70, s38
	v_or_b32_e32 v69, 33, v106
	v_or_b32_e32 v70, 34, v106
	v_or_b32_e32 v72, 32, v106
	v_cmp_gt_u32_e64 s[12:13], v72, v102
	v_cmp_gt_u32_e64 s[14:15], v69, v102
	v_cmp_gt_u32_e64 s[18:19], v70, v102
	v_cmp_gt_u32_e64 s[22:23], v71, v102
	v_cndmask_b32_e64 v72, v78, 0, s[12:13]
	v_cndmask_b32_e64 v69, v79, 0, s[14:15]
	v_cndmask_b32_e64 v70, v80, 0, s[18:19]
	v_cndmask_b32_e64 v71, v81, 0, s[22:23]
	v_perm_b32 v86, v69, v72, s38
	v_perm_b32 v87, v71, v70, s38
	v_or_b32_e32 v69, 49, v106
	v_or_b32_e32 v70, 48, v106
	v_cmp_gt_u32_e64 s[24:25], v70, v102
	v_cmp_gt_u32_e64 s[26:27], v69, v102
	s_nop 0
	v_cndmask_b32_e64 v66, v66, 0, s[24:25]
	v_cndmask_b32_e64 v67, v67, 0, s[26:27]
	v_perm_b32 v88, v67, v66, s38
	v_or_b32_e32 v66, 50, v106
	v_cmp_gt_u32_e64 s[28:29], v66, v102
	v_lshrrev_b32_e32 v67, 1, v104
	v_bfe_u32 v66, v0, 1, 3
	v_cndmask_b32_e64 v121, v68, 0, s[28:29]
	v_lshrrev_b32_e32 v68, 1, v0
	v_bitop3_b32 v69, v67, v68, 7 bitop3:0x78
	v_and_b32_e32 v111, 8, v68
	v_lshlrev_b32_e32 v109, 4, v69
	v_add3_u32 v70, s30, v111, v112
	v_add_u32_e32 v128, v70, v109
	ds_read2st64_b64 v[90:93], v128 offset1:4
	v_bitop3_b32 v68, v67, v66, 2 bitop3:0x36
	v_lshlrev_b32_e32 v110, 4, v68
	v_bitop3_b32 v71, v67, v66, 4 bitop3:0x36
	v_bitop3_b32 v72, v67, v66, 6 bitop3:0x36
	s_waitcnt lgkmcnt(0)
	v_mov_b32_e32 v82, v90
	v_add_u32_e32 v90, v70, v110
	ds_read2st64_b64 v[66:69], v90 offset1:4
	v_lshlrev_b32_e32 v107, 4, v71
	v_lshlrev_b32_e32 v108, 4, v72
	v_add_u32_e32 v136, v70, v107
	v_add_u32_e32 v140, v70, v108
	ds_read2st64_b64 v[94:97], v136 offset1:4
	ds_read2st64_b64 v[70:73], v140 offset1:4
	v_mov_b32_e32 v83, v91
	s_waitcnt lgkmcnt(0)
	v_mov_b32_e32 v84, v66
	v_mov_b32_e32 v85, v67
	v_mov_b32_e32 v78, v94
	v_mov_b32_e32 v79, v95
	v_mov_b32_e32 v80, v70
	v_mov_b32_e32 v81, v71
	v_mfma_f32_16x16x32_bf16 v[98:101], v[82:85], v[74:77], 0
	v_cmp_gt_u32_e64 s[30:31], v120, v102
	v_mov_b32_e32 v67, v93
	v_mov_b32_e32 v70, v96
	v_cndmask_b32_e64 v66, v89, 0, s[30:31]
	v_perm_b32 v89, v66, v121, s38
	v_mov_b32_e32 v66, v92
	ds_read_b128 v[120:123], v114 offset:32768
	ds_read_b128 v[124:127], v114 offset:40960
	v_mfma_f32_16x16x32_bf16 v[98:101], v[78:81], v[86:89], v[98:101]
	v_mov_b32_e32 v71, v97
	ds_read2st64_b64 v[128:131], v128 offset0:8 offset1:12
	ds_read2st64_b64 v[90:93], v90 offset0:8 offset1:12
	ds_read2st64_b64 v[136:139], v136 offset0:8 offset1:12
	s_waitcnt lgkmcnt(0)
	v_mfma_f32_16x16x32_bf16 v[120:123], v[120:123], v[62:65], v[98:101]
	v_mov_b32_e32 v94, v128
	v_mov_b32_e32 v95, v129
	v_mfma_f32_16x16x32_bf16 v[98:101], v[66:69], v[74:77], 0
	v_mov_b32_e32 v96, v90
	v_mov_b32_e32 v97, v91
	v_mov_b32_e32 v90, v130
	v_mfma_f32_16x16x32_bf16 v[132:135], v[70:73], v[86:89], v[98:101]
	v_mov_b32_e32 v91, v131
	s_nop 2
	ds_read2st64_b64 v[98:101], v140 offset0:8 offset1:12
	v_mfma_f32_16x16x32_bf16 v[124:127], v[124:127], v[62:65], v[132:135]
	ds_read_b128 v[144:147], v114 offset:49152
	ds_read_b128 v[148:151], v114 offset:57344
	ds_read_b128 v[128:131], v115 offset:32768
	v_mov_b32_e32 v132, v136
	v_mov_b32_e32 v133, v137
	s_waitcnt lgkmcnt(0)
	v_mov_b32_e32 v134, v98
	v_mov_b32_e32 v135, v99
	v_mov_b32_e32 v98, v138
	v_mov_b32_e32 v99, v139
	v_mfma_f32_16x16x32_bf16 v[140:143], v[94:97], v[74:77], 0
	v_mfma_f32_16x16x32_bf16 v[74:77], v[90:93], v[74:77], 0
	v_mfma_f32_16x16x32_bf16 v[140:143], v[132:135], v[86:89], v[140:143]
	v_mfma_f32_16x16x32_bf16 v[74:77], v[98:101], v[86:89], v[74:77]
	ds_read_b128 v[86:89], v117 offset:32768
	v_mfma_f32_16x16x32_bf16 v[140:143], v[144:147], v[62:65], v[140:143]
	v_mfma_f32_16x16x32_bf16 v[62:65], v[148:151], v[62:65], v[74:77]
	s_nop 4
	ds_read_b128 v[74:77], v117 offset:40960
	s_waitcnt lgkmcnt(0)
	v_mfma_f32_16x16x32_bf16 v[86:89], v[86:89], v[58:61], v[120:123]
	s_nop 2
	ds_read_b128 v[120:123], v117 offset:49152
	v_mfma_f32_16x16x32_bf16 v[74:77], v[74:77], v[58:61], v[124:127]
	s_nop 2
	ds_read_b128 v[124:127], v117 offset:57344
	s_waitcnt lgkmcnt(0)
	v_mfma_f32_16x16x32_bf16 v[120:123], v[120:123], v[58:61], v[140:143]
	v_mfma_f32_16x16x32_bf16 v[58:61], v[124:127], v[58:61], v[62:65]
	ds_read_b128 v[124:127], v115 offset:49152
	s_nop 1
	ds_read_b128 v[62:65], v115 offset:40960
	s_waitcnt lgkmcnt(0)
	v_mfma_f32_16x16x32_bf16 v[62:65], v[62:65], v[54:57], v[74:77]
	s_nop 2
	ds_read_b128 v[74:77], v115 offset:57344
	v_cndmask_b32_e64 v115, 0, 1.0, s[0:1]
	v_mfma_f32_16x16x32_bf16 v[120:123], v[124:127], v[54:57], v[120:123]
	ds_read_b128 v[124:127], v113 offset:32768
	v_mfma_f32_16x16x32_bf16 v[86:89], v[128:131], v[54:57], v[86:89]
	s_waitcnt lgkmcnt(0)
	v_mfma_f32_16x16x32_bf16 v[54:57], v[74:77], v[54:57], v[58:61]
	s_nop 2
	ds_read_b128 v[58:61], v113 offset:40960
	v_mfma_f32_16x16x32_bf16 v[74:77], v[124:127], v[50:53], v[86:89]
	s_nop 2
	ds_read_b128 v[86:89], v113 offset:49152
	s_waitcnt lgkmcnt(0)
	v_mfma_f32_16x16x32_bf16 v[58:61], v[58:61], v[50:53], v[62:65]
	s_nop 2
	ds_read_b128 v[62:65], v113 offset:57344
	v_mov_b32_e32 v113, 0x3f80
	v_cndmask_b32_e64 v114, v113, 0, vcc
	v_mfma_f32_16x16x32_bf16 v[86:89], v[86:89], v[50:53], v[120:123]
	s_nop 2
	ds_read_b128 v[120:123], v119 offset:32768
	s_waitcnt lgkmcnt(0)
	v_mfma_f32_16x16x32_bf16 v[50:53], v[62:65], v[50:53], v[54:57]
	s_nop 2
	ds_read_b128 v[54:57], v119 offset:40960
	v_mfma_f32_16x16x32_bf16 v[62:65], v[120:123], v[46:49], v[74:77]
	s_nop 2
	ds_read_b128 v[74:77], v119 offset:49152
	s_waitcnt lgkmcnt(0)
	v_mfma_f32_16x16x32_bf16 v[74:77], v[74:77], v[46:49], v[86:89]
	s_nop 2
	ds_read_b128 v[86:89], v118 offset:32768
	v_mfma_f32_16x16x32_bf16 v[54:57], v[54:57], v[46:49], v[58:61]
	s_nop 2
	ds_read_b128 v[58:61], v119 offset:57344
	s_waitcnt lgkmcnt(0)
	v_mfma_f32_16x16x32_bf16 v[46:49], v[58:61], v[46:49], v[50:53]
	s_nop 2
	ds_read_b128 v[50:53], v118 offset:40960
	v_mfma_f32_16x16x32_bf16 v[58:61], v[86:89], v[42:45], v[62:65]
	s_nop 2
	ds_read_b128 v[62:65], v118 offset:49152
	s_waitcnt lgkmcnt(0)
	v_mfma_f32_16x16x32_bf16 v[62:65], v[62:65], v[42:45], v[74:77]
	s_nop 2
	ds_read_b128 v[74:77], v116 offset:32768
	v_mfma_f32_16x16x32_bf16 v[50:53], v[50:53], v[42:45], v[54:57]
	s_nop 2
	ds_read_b128 v[54:57], v118 offset:57344
	s_waitcnt lgkmcnt(0)
	v_mfma_f32_16x16x32_bf16 v[42:45], v[54:57], v[42:45], v[46:49]
	s_nop 2
	ds_read_b128 v[46:49], v116 offset:40960
	ds_read_b128 v[54:57], v116 offset:49152
	ds_read_b128 v[86:89], v116 offset:57344
	v_cndmask_b32_e64 v116, v113, 0, s[4:5]
	v_mfma_f32_16x16x32_bf16 v[58:61], v[74:77], v[38:41], v[58:61]
	s_waitcnt lgkmcnt(0)
	v_mfma_f32_16x16x32_bf16 v[46:49], v[46:49], v[38:41], v[50:53]
	s_nop 2
	ds_read_b128 v[50:53], v1 offset:32768
	ds_read_b128 v[74:77], v1 offset:40960
	v_mfma_f32_16x16x32_bf16 v[54:57], v[54:57], v[38:41], v[62:65]
	v_mfma_f32_16x16x32_bf16 v[38:41], v[86:89], v[38:41], v[42:45]
	v_cndmask_b32_e64 v87, v113, 0, s[12:13]
	s_nop 0
	v_cndmask_b32_e64 v62, 1.0, 0, s[6:7]
	v_cndmask_b32_e64 v63, v113, 0, s[8:9]
	ds_read_b128 v[42:45], v1 offset:49152
	s_waitcnt lgkmcnt(0)
	v_mfma_f32_16x16x32_bf16 v[50:53], v[50:53], v[34:37], v[58:61]
	v_cndmask_b32_e64 v64, 1.0, 0, s[10:11]
	v_cndmask_b32_e64 v65, v113, 0, s[16:17]
	v_cndmask_b32_e64 v86, 1.0, 0, s[20:21]
	ds_read_b128 v[58:61], v1 offset:57344
	v_cndmask_b32_e64 v1, 1.0, 0, s[14:15]
	v_mfma_f32_16x16x32_bf16 v[46:49], v[74:77], v[34:37], v[46:49]
	v_cndmask_b32_e64 v74, v113, 0, s[18:19]
	v_cndmask_b32_e64 v75, 1.0, 0, s[22:23]
	v_cndmask_b32_e64 v76, v113, 0, s[24:25]
	v_mfma_f32_16x16x32_bf16 v[42:45], v[42:45], v[34:37], v[54:57]
	v_cndmask_b32_e64 v77, 1.0, 0, s[26:27]
	v_cndmask_b32_e64 v88, v113, 0, s[28:29]
	v_cndmask_b32_e64 v89, 1.0, 0, s[30:31]
	s_waitcnt lgkmcnt(0)
	v_mfma_f32_16x16x32_bf16 v[38:41], v[58:61], v[34:37], v[38:41]
	v_or_b32_e32 v34, v1, v87
	v_add3_u32 v1, s34, v111, v112
	v_add_u32_e32 v113, v1, v109
	v_add_u32_e32 v118, v1, v110
	v_or_b32_e32 v55, v62, v116
	v_or_b32_e32 v56, v64, v63
	v_or_b32_e32 v57, v86, v65
	v_or_b32_e32 v35, v75, v74
	ds_read2st64_b64 v[62:65], v113 offset1:4
	v_or_b32_e32 v36, v77, v76
	ds_read2st64_b64 v[74:77], v118 offset1:4
	v_add_u32_e32 v119, v1, v107
	v_add_u32_e32 v1, v1, v108
	v_or_b32_e32 v54, v115, v114
	v_or_b32_e32 v37, v89, v88
	ds_read2st64_b64 v[86:89], v119 offset1:4
	ds_read2st64_b64 v[114:117], v1 offset1:4
	v_mfma_f32_16x16x32_bf16 v[58:61], v[82:85], v[54:57], 0
	s_waitcnt lgkmcnt(0)
	v_mov_b32_e32 v82, v62
	v_mov_b32_e32 v83, v63
	v_mov_b32_e32 v84, v74
	v_mov_b32_e32 v85, v75
	v_mfma_f32_16x16x32_bf16 v[66:69], v[66:69], v[54:57], 0
	v_mov_b32_e32 v74, v64
	v_mov_b32_e32 v75, v65
	ds_read2st64_b64 v[62:65], v113 offset0:8 offset1:12
	v_mfma_f32_16x16x32_bf16 v[58:61], v[78:81], v[34:37], v[58:61]
	v_mov_b32_e32 v78, v86
	v_mov_b32_e32 v79, v87
	v_mov_b32_e32 v80, v114
	v_mov_b32_e32 v81, v115
	v_mfma_f32_16x16x32_bf16 v[82:85], v[82:85], v[54:57], 0
	v_mov_b32_e32 v114, v88
	v_mov_b32_e32 v115, v89
	v_mul_f32_e32 v51, 0x3d800000, v51
	v_mfma_f32_16x16x32_bf16 v[66:69], v[70:73], v[34:37], v[66:69]
	v_mul_f32_e32 v52, 0x3d800000, v52
	v_mul_f32_e32 v53, 0x3d800000, v53
	s_mov_b32 s34, 0xff61b1e6
	v_mfma_f32_16x16x32_bf16 v[70:73], v[94:97], v[54:57], 0
	v_mul_f32_e32 v46, 0x3d800000, v46
	s_nop 2
	v_add_f32_e32 v86, v66, v26
	v_add_f32_e32 v87, v67, v27
	v_mfma_f32_16x16x32_bf16 v[78:81], v[78:81], v[34:37], v[82:85]
	v_add_f32_e32 v94, v68, v28
	v_add_f32_e32 v95, v69, v29
	ds_read2st64_b64 v[66:69], v119 offset0:8 offset1:12
	v_add_f32_e32 v82, v58, v30
	v_add_f32_e32 v83, v59, v31
	v_add_f32_e32 v84, v60, v32
	v_add_f32_e32 v85, v61, v33
	v_mfma_f32_16x16x32_bf16 v[30:33], v[132:135], v[34:37], v[70:73]
	v_mul_f32_e32 v47, 0x3d800000, v47
	v_mul_f32_e32 v48, 0x3d800000, v48
	v_mul_f32_e32 v49, 0x3d800000, v49
	v_mfma_f32_16x16x32_bf16 v[26:29], v[90:93], v[54:57], 0
	ds_read2st64_b64 v[70:73], v1 offset0:8 offset1:12
	s_nop 2
	v_add_f32_e32 v90, v30, v22
	v_add_f32_e32 v91, v31, v23
	v_add_f32_e32 v92, v32, v24
	v_add_f32_e32 v88, v33, v25
	ds_read2st64_b64 v[22:25], v118 offset0:8 offset1:12
	v_mfma_f32_16x16x32_bf16 v[58:61], v[74:77], v[54:57], 0
	s_waitcnt lgkmcnt(0)
	v_mov_b32_e32 v74, v66
	v_mov_b32_e32 v75, v67
	v_mov_b32_e32 v76, v70
	v_mfma_f32_16x16x32_bf16 v[30:33], v[114:117], v[34:37], v[58:61]
	v_mov_b32_e32 v77, v71
	v_mov_b32_e32 v70, v68
	v_add_f32_e32 v68, v79, v15
	v_mov_b32_e32 v58, v62
	v_mov_b32_e32 v59, v63
	v_mov_b32_e32 v60, v22
	v_mov_b32_e32 v61, v23
	v_mfma_f32_16x16x32_bf16 v[26:29], v[98:101], v[34:37], v[26:29]
	v_rcp_f32_e32 v62, v85
	v_rcp_f32_e32 v63, v86
	v_rcp_f32_e32 v79, v87
	v_mfma_f32_16x16x32_bf16 v[58:61], v[58:61], v[54:57], 0
	v_mov_b32_e32 v71, v69
	s_nop 2
	v_add_f32_e32 v26, v26, v18
	v_add_f32_e32 v1, v27, v19
	v_add_f32_e32 v27, v28, v20
	v_add_f32_e32 v28, v29, v21
	v_mfma_f32_16x16x32_bf16 v[18:21], v[74:77], v[34:37], v[58:61]
	v_mul_f32_e32 v29, 0x3d800000, v50
	v_rcp_f32_e32 v50, v82
	v_add_f32_e32 v69, v80, v16
	v_rcp_f32_e32 v60, v83
	v_rcp_f32_e32 v61, v84
	v_add_f32_e32 v74, v81, v17
	v_rcp_f32_e32 v80, v94
	v_rcp_f32_e32 v81, v95
	v_add_f32_e32 v75, v30, v10
	v_add_f32_e32 v76, v31, v11
	v_mul_f32_e32 v30, 0x3d800000, v42
	v_mul_f32_e32 v31, 0x3d800000, v43
	v_add_f32_e32 v42, v18, v6
	v_add_f32_e32 v43, v19, v7
	v_mul_f32_e32 v18, v29, v50
	v_mul_f32_e32 v19, v51, v60
	v_rcp_f32_e32 v82, v90
	v_rcp_f32_e32 v83, v91
	v_add_f32_e32 v77, v32, v12
	v_mul_f32_e32 v32, 0x3d800000, v44
	v_add_f32_e32 v44, v20, v8
	v_max3_f32 v18, v18, s34, v19
	v_mul_f32_e32 v19, v52, v61
	v_mul_f32_e32 v20, v53, v62
	v_rcp_f32_e32 v84, v92
	v_rcp_f32_e32 v85, v88
	v_max3_f32 v18, v18, v19, v20
	v_mul_f32_e32 v19, v46, v63
	v_mul_f32_e32 v20, v47, v79
	v_rcp_f32_e32 v86, v26
	v_rcp_f32_e32 v87, v1
	v_max3_f32 v18, v18, v19, v20
	v_mul_f32_e32 v19, v48, v80
	v_mul_f32_e32 v20, v49, v81
	v_rcp_f32_e32 v88, v27
	v_rcp_f32_e32 v89, v28
	v_add_f32_e32 v67, v78, v14
	v_add_f32_e32 v78, v33, v13
	v_mul_f32_e32 v33, 0x3d800000, v45
	v_max3_f32 v18, v18, v19, v20
	v_mul_f32_e32 v19, v30, v82
	v_mul_f32_e32 v20, v31, v83
	v_max3_f32 v18, v18, v19, v20
	v_mul_f32_e32 v19, v32, v84
	v_mul_f32_e32 v20, v33, v85
	v_mul_f32_e32 v38, 0x3d800000, v38
	v_mul_f32_e32 v39, 0x3d800000, v39
	v_max3_f32 v18, v18, v19, v20
	v_mul_f32_e32 v1, v38, v86
	v_mul_f32_e32 v19, v39, v87
	v_mul_f32_e32 v40, 0x3d800000, v40
	v_mul_f32_e32 v41, 0x3d800000, v41
	v_max3_f32 v1, v18, v1, v19
	v_mul_f32_e32 v18, v40, v88
	v_mul_f32_e32 v19, v41, v89
	v_max3_f32 v1, v1, v18, v19
	v_mbcnt_lo_u32_b32 v18, -1, 0
	v_mbcnt_hi_u32_b32 v26, -1, v18
	v_and_b32_e32 v19, 64, v26
	v_xor_b32_e32 v18, 16, v26
	v_add_u32_e32 v27, 64, v19
	v_cmp_lt_i32_e64 s[34:35], v18, v27
	v_mov_b32_e32 v22, v64
	v_mov_b32_e32 v23, v65
	v_cndmask_b32_e64 v18, v26, v18, s[34:35]
	v_lshlrev_b32_e32 v64, 2, v18
	ds_bpermute_b32 v28, v64, v1
	v_add_f32_e32 v45, v21, v9
	v_mfma_f32_16x16x32_bf16 v[18:21], v[22:25], v[54:57], 0
	v_lshlrev_b32_e32 v58, 9, v102
	v_mov_b32_e32 v59, 0
	s_waitcnt lgkmcnt(0)
	v_max_f32_e32 v24, v28, v28
	v_max_f32_e32 v24, v1, v24
	v_xor_b32_e32 v1, 32, v26
	v_cmp_lt_i32_e64 s[34:35], v1, v27
	v_lshl_add_u64 v[22:23], s[36:37], 0, v[58:59]
	v_lshlrev_b32_e32 v58, 3, v104
	v_cndmask_b32_e64 v1, v26, v1, s[34:35]
	v_lshlrev_b32_e32 v65, 2, v1
	ds_bpermute_b32 v25, v65, v24
	v_lshl_add_u64 v[22:23], v[22:23], 0, v[58:59]
	v_and_b32_e32 v58, 0x100, v0
	v_lshrrev_b32_e32 v66, 8, v0
	v_lshl_add_u64 v[0:1], v[22:23], 0, v[58:59]
	s_waitcnt lgkmcnt(0)
	v_max_f32_e32 v22, v25, v25
	v_max_f32_e32 v54, v24, v22
	v_fma_f32 v22, v29, v50, -v54
	v_mul_f32_e32 v22, 0x3fb8aa3b, v22
	v_fma_f32 v23, v51, v60, -v54
	v_exp_f32_e32 v22, v22
	v_mul_f32_e32 v23, 0x3fb8aa3b, v23
	v_fma_f32 v24, v52, v61, -v54
	v_exp_f32_e32 v23, v23
	v_mul_f32_e32 v24, 0x3fb8aa3b, v24
	v_fma_f32 v25, v53, v62, -v54
	v_exp_f32_e32 v24, v24
	v_mul_f32_e32 v25, 0x3fb8aa3b, v25
	v_fma_f32 v26, v46, v63, -v54
	v_exp_f32_e32 v25, v25
	v_mul_f32_e32 v26, 0x3fb8aa3b, v26
	v_fma_f32 v27, v47, v79, -v54
	v_exp_f32_e32 v26, v26
	v_mul_f32_e32 v27, 0x3fb8aa3b, v27
	v_fma_f32 v28, v48, v80, -v54
	v_add_f32_e32 v46, 0, v22
	v_exp_f32_e32 v27, v27
	v_mul_f32_e32 v28, 0x3fb8aa3b, v28
	v_fma_f32 v29, v49, v81, -v54
	v_add_f32_e32 v46, v46, v23
	v_exp_f32_e32 v28, v28
	v_mul_f32_e32 v29, 0x3fb8aa3b, v29
	v_add_f32_e32 v46, v46, v24
	v_fma_f32 v30, v30, v82, -v54
	v_exp_f32_e32 v29, v29
	v_add_f32_e32 v46, v46, v25
	v_mul_f32_e32 v30, 0x3fb8aa3b, v30
	v_fma_f32 v31, v31, v83, -v54
	v_add_f32_e32 v46, v46, v26
	v_exp_f32_e32 v30, v30
	v_mul_f32_e32 v31, 0x3fb8aa3b, v31
	v_fma_f32 v32, v32, v84, -v54
	v_add_f32_e32 v46, v46, v27
	v_exp_f32_e32 v31, v31
	v_mul_f32_e32 v32, 0x3fb8aa3b, v32
	v_fma_f32 v33, v33, v85, -v54
	v_add_f32_e32 v46, v46, v28
	v_exp_f32_e32 v32, v32
	v_mul_f32_e32 v33, 0x3fb8aa3b, v33
	v_fma_f32 v38, v38, v86, -v54
	v_add_f32_e32 v46, v46, v29
	v_exp_f32_e32 v33, v33
	v_mul_f32_e32 v38, 0x3fb8aa3b, v38
	v_fma_f32 v39, v39, v87, -v54
	v_add_f32_e32 v46, v46, v30
	v_exp_f32_e32 v38, v38
	v_mul_f32_e32 v39, 0x3fb8aa3b, v39
	v_fma_f32 v40, v40, v88, -v54
	v_add_f32_e32 v46, v46, v31
	v_exp_f32_e32 v39, v39
	v_mul_f32_e32 v40, 0x3fb8aa3b, v40
	v_fma_f32 v41, v41, v89, -v54
	v_add_f32_e32 v46, v46, v32
	v_exp_f32_e32 v40, v40
	v_mul_f32_e32 v41, 0x3fb8aa3b, v41
	v_add_f32_e32 v46, v46, v33
	v_exp_f32_e32 v41, v41
	v_add_f32_e32 v46, v46, v38
	v_add_f32_e32 v46, v46, v39
	v_add_f32_e32 v46, v46, v40
	v_add_f32_e32 v58, v46, v41
	ds_bpermute_b32 v79, v64, v58
	global_load_dwordx2 v[62:63], v[0:1], off
	global_load_dwordx2 v[60:61], v[0:1], off offset:32
	global_load_dwordx2 v[56:57], v[0:1], off offset:64
	global_load_dwordx2 v[52:53], v[0:1], off offset:96
	global_load_dwordx2 v[54:55], v[0:1], off offset:128
	global_load_dwordx2 v[50:51], v[0:1], off offset:160
	global_load_dwordx2 v[48:49], v[0:1], off offset:192
	global_load_dwordx2 v[46:47], v[0:1], off offset:224
	v_mfma_f32_16x16x32_bf16 v[18:21], v[70:73], v[34:37], v[18:21]
	v_rcp_f32_e32 v34, v75
	s_waitcnt lgkmcnt(0)
	v_add_f32_e32 v0, v58, v79
	ds_bpermute_b32 v1, v65, v0
	v_rcp_f32_e32 v35, v76
	v_rcp_f32_e32 v36, v77
	s_nop 1
	v_add_f32_e32 v58, v18, v2
	v_rcp_f32_e32 v18, v67
	s_waitcnt lgkmcnt(0)
	v_add_f32_e32 v0, v0, v1
	v_rcp_f32_e32 v0, v0
	v_add_f32_e32 v1, v19, v3
	v_rcp_f32_e32 v19, v68
	v_add_f32_e32 v70, v20, v4
	v_add_f32_e32 v71, v21, v5
	v_rcp_f32_e32 v20, v69
	v_rcp_f32_e32 v21, v74
	v_mul_f32_e32 v0, 0x43800000, v0
	v_pk_mul_f32 v[22:23], v[0:1], v[22:23] op_sel_hi:[0,1]
	v_pk_mul_f32 v[18:19], v[22:23], v[18:19]
	v_pk_mul_f32 v[22:23], v[0:1], v[24:25] op_sel_hi:[0,1]
	v_pk_mul_f32 v[20:21], v[22:23], v[20:21]
	v_rcp_f32_e32 v37, v78
	v_pk_mul_f32 v[14:15], v[14:15], v[18:19]
	v_pk_mul_f32 v[16:17], v[16:17], v[20:21]
	v_cvt_pk_f16_f32 v14, v14, v15
	v_cvt_pk_f16_f32 v15, v16, v17
	v_pk_mul_f32 v[16:17], v[0:1], v[26:27] op_sel_hi:[0,1]
	v_pk_mul_f32 v[16:17], v[16:17], v[34:35]
	v_cvt_pk_bf16_f32 v18, v18, v19
	v_cvt_pk_bf16_f32 v19, v20, v21
	v_pk_mul_f32 v[10:11], v[10:11], v[16:17]
	v_cvt_pk_bf16_f32 v20, v16, v17
	v_pk_mul_f32 v[16:17], v[0:1], v[28:29] op_sel_hi:[0,1]
	v_pk_mul_f32 v[72:73], v[16:17], v[36:37]
	v_rcp_f32_e32 v16, v42
	v_rcp_f32_e32 v17, v43
	v_rcp_f32_e32 v24, v44
	v_rcp_f32_e32 v25, v45
	v_rcp_f32_e32 v26, v58
	v_rcp_f32_e32 v27, v1
	v_pk_mul_f32 v[22:23], v[0:1], v[30:31] op_sel_hi:[0,1]
	v_pk_mul_f32 v[76:77], v[22:23], v[16:17]
	v_pk_mul_f32 v[16:17], v[0:1], v[32:33] op_sel_hi:[0,1]
	v_pk_mul_f32 v[78:79], v[16:17], v[24:25]
	v_pk_mul_f32 v[16:17], v[0:1], v[38:39] op_sel_hi:[0,1]
	s_add_i32 s34, 0, 0x24000
	v_pk_mul_f32 v[80:81], v[16:17], v[26:27]
	v_add3_u32 v16, s34, v112, v111
	v_add_u32_e32 v17, v16, v109
	v_add_u32_e32 v58, v16, v110
	s_barrier
	ds_write_b128 v152, v[70:73]
	ds_write_b128 v152, v[76:79] offset:1024
	ds_write_b64 v153, v[0:1] offset:2048
	ds_write_b64 v153, v[10:11] offset:2560
	ds_write_b64 v153, v[14:15] offset:3072
	ds_write_b64 v153, v[18:19] offset:3584
	ds_write_b64 v153, v[40:41] offset:4096
	ds_write_b64 v153, v[80:81] offset:4608
	ds_write_b32 v154, v20 offset:5120
	s_waitcnt lgkmcnt(0)
	s_branch .Lat_join
.Lat_dh1:
	s_add_u32 s36, s30, s34
	s_addc_u32 s37, s31, s35
	v_lshlrev_b32_e32 v112, 7, v103
	v_lshlrev_b32_e32 v106, 2, v104
	v_cmp_gt_u32_e32 vcc, v106, v102
	s_nop 1
	v_or_b32_e32 v74, 3, v106
	v_cmp_gt_u32_e64 s[6:7], v74, v102
	s_nop 1
	v_or_b32_e32 v120, 51, v106
	v_or_b32_e32 v69, 2, v106
	v_cmp_lt_u32_e64 s[0:1], v106, v102
	s_nop 1
	v_cmp_gt_u32_e64 s[4:5], v69, v102
	s_nop 1
	v_or_b32_e32 v69, 17, v106
	v_or_b32_e32 v76, 16, v106
	v_cmp_gt_u32_e64 s[8:9], v76, v102
	s_nop 1
	v_cmp_gt_u32_e64 s[10:11], v69, v102
	s_nop 1
	v_or_b32_e32 v69, 19, v106
	v_or_b32_e32 v70, 18, v106
	v_cmp_gt_u32_e64 s[16:17], v70, v102
	s_nop 1
	v_cmp_gt_u32_e64 s[20:21], v69, v102
	s_nop 1
	v_or_b32_e32 v71, 35, v106
	v_or_b32_e32 v69, 33, v106
	v_or_b32_e32 v70, 34, v106
	v_or_b32_e32 v72, 32, v106
	v_cmp_gt_u32_e64 s[12:13], v72, v102
	s_nop 1
	v_cmp_gt_u32_e64 s[14:15], v69, v102
	s_nop 1
	v_cmp_gt_u32_e64 s[18:19], v70, v102
	s_nop 1
	v_cmp_gt_u32_e64 s[22:23], v71, v102
	s_nop 1
	v_or_b32_e32 v69, 49, v106
	v_or_b32_e32 v70, 48, v106
	v_cmp_gt_u32_e64 s[24:25], v70, v102
	s_nop 1
	v_cmp_gt_u32_e64 s[26:27], v69, v102
	s_nop 1
	v_or_b32_e32 v66, 50, v106
	v_cmp_gt_u32_e64 s[28:29], v66, v102
	s_nop 1
	v_lshrrev_b32_e32 v67, 1, v104
	v_bfe_u32 v66, v0, 1, 3
	v_lshrrev_b32_e32 v68, 1, v0
	v_bitop3_b32 v69, v67, v68, 7 bitop3:0x78
	v_and_b32_e32 v111, 8, v68
	v_lshlrev_b32_e32 v109, 4, v69
	v_bitop3_b32 v68, v67, v66, 2 bitop3:0x36
	v_lshlrev_b32_e32 v110, 4, v68
	v_bitop3_b32 v71, v67, v66, 4 bitop3:0x36
	v_bitop3_b32 v72, v67, v66, 6 bitop3:0x36
	v_lshlrev_b32_e32 v107, 4, v71
	v_lshlrev_b32_e32 v108, 4, v72
	v_cmp_gt_u32_e64 s[30:31], v120, v102
	s_nop 1
	v_mbcnt_lo_u32_b32 v18, -1, 0
	v_mbcnt_hi_u32_b32 v26, -1, v18
	v_and_b32_e32 v19, 64, v26
	v_xor_b32_e32 v18, 16, v26
	v_add_u32_e32 v27, 64, v19
	v_cmp_lt_i32_e64 s[34:35], v18, v27
	s_nop 1
	v_cndmask_b32_e64 v18, v26, v18, s[34:35]
	v_lshlrev_b32_e32 v64, 2, v18
	v_lshlrev_b32_e32 v58, 9, v102
	v_mov_b32_e32 v59, 0
	v_xor_b32_e32 v1, 32, v26
	v_cmp_lt_i32_e64 s[34:35], v1, v27
	s_nop 1
	v_lshl_add_u64 v[22:23], s[36:37], 0, v[58:59]
	v_lshlrev_b32_e32 v58, 3, v104
	v_cndmask_b32_e64 v1, v26, v1, s[34:35]
	v_lshlrev_b32_e32 v65, 2, v1
	v_lshl_add_u64 v[22:23], v[22:23], 0, v[58:59]
	v_and_b32_e32 v58, 0x100, v0
	v_lshrrev_b32_e32 v66, 8, v0
	v_lshl_add_u64 v[0:1], v[22:23], 0, v[58:59]
	global_load_dwordx2 v[62:63], v[0:1], off
	global_load_dwordx2 v[60:61], v[0:1], off offset:32
	global_load_dwordx2 v[56:57], v[0:1], off offset:64
	global_load_dwordx2 v[52:53], v[0:1], off offset:96
	global_load_dwordx2 v[54:55], v[0:1], off offset:128
	global_load_dwordx2 v[50:51], v[0:1], off offset:160
	global_load_dwordx2 v[48:49], v[0:1], off offset:192
	global_load_dwordx2 v[46:47], v[0:1], off offset:224
	s_add_i32 s34, 0, 0x24000
	v_add3_u32 v16, s34, v112, v111
	v_add_u32_e32 v17, v16, v109
	v_add_u32_e32 v58, v16, v110
	s_barrier
.Lat_join:
	s_waitcnt vmcnt(0)
	s_barrier
	s_cmp_lt_u32 s44, 0x100
	s_cbranch_scc1 .Lat_cont
	ds_read_b128 v[70:73], v152
	ds_read_b128 v[76:79], v152 offset:1024
	ds_read_b64 v[0:1], v153 offset:2048
	ds_read_b64 v[10:11], v153 offset:2560
	ds_read_b64 v[14:15], v153 offset:3072
	ds_read_b64 v[18:19], v153 offset:3584
	ds_read_b64 v[40:41], v153 offset:4096
	ds_read_b64 v[80:81], v153 offset:4608
	ds_read_b32 v20, v154 offset:5120
	s_waitcnt lgkmcnt(0)
.Lat_cont:
	ds_read2st64_b64 v[26:29], v17 offset1:4
	ds_read2st64_b64 v[30:33], v58 offset1:4
	v_rcp_f32_e32 v34, v70
	v_rcp_f32_e32 v35, v71
	v_add_u32_e32 v67, v16, v107
	v_add_u32_e32 v74, v16, v108
	v_pk_mul_f32 v[0:1], v[0:1], v[40:41] op_sel_hi:[0,1]
	ds_read2st64_b64 v[38:41], v67 offset1:4
	ds_read2st64_b64 v[42:45], v74 offset1:4
	v_pk_mul_f32 v[84:85], v[0:1], v[34:35]
	s_waitcnt lgkmcnt(0)
	v_mov_b32_e32 v34, v26
	v_mov_b32_e32 v35, v27
	v_mov_b32_e32 v36, v30
	v_mov_b32_e32 v37, v31
	v_mov_b32_e32 v30, v28
	v_mov_b32_e32 v31, v29
	v_cvt_pk_bf16_f32 v21, v72, v73
	v_mov_b32_e32 v68, v38
	v_mov_b32_e32 v69, v39
	v_mov_b32_e32 v70, v42
	v_mov_b32_e32 v71, v43
	v_mov_b32_e32 v42, v40
	v_mov_b32_e32 v43, v41
	v_mfma_f32_16x16x32_bf16 v[34:37], v[34:37], v[18:21], 0
	v_cvt_pk_bf16_f32 v22, v76, v77
	v_cvt_pk_bf16_f32 v23, v78, v79
	v_cvt_pk_bf16_f32 v24, v80, v81
	v_mfma_f32_16x16x32_bf16 v[30:33], v[30:33], v[18:21], 0
	v_cvt_pk_bf16_f32 v25, v84, v85
	v_cvt_pk_f16_f32 v16, v10, v11
	v_pk_mul_f32 v[0:1], v[12:13], v[72:73]
	v_mfma_f32_16x16x32_bf16 v[26:29], v[68:71], v[22:25], v[34:37]
	ds_read2st64_b64 v[68:71], v74 offset0:8 offset1:12
	v_pk_mul_f32 v[2:3], v[2:3], v[80:81]
	v_pk_mul_f32 v[4:5], v[4:5], v[84:85]
	ds_read2st64_b64 v[34:37], v17 offset0:8 offset1:12
	v_mfma_f32_16x16x32_bf16 v[10:13], v[42:45], v[22:25], v[30:33]
	ds_read2st64_b64 v[42:45], v67 offset0:8 offset1:12
	s_waitcnt lgkmcnt(0)
	v_mov_b32_e32 v74, v68
	v_mov_b32_e32 v75, v69
	ds_read2st64_b64 v[30:33], v58 offset0:8 offset1:12
	v_mov_b32_e32 v38, v34
	v_mov_b32_e32 v39, v35
	v_mov_b32_e32 v72, v42
	v_mov_b32_e32 v73, v43
	s_waitcnt lgkmcnt(0)
	v_mov_b32_e32 v40, v30
	v_mov_b32_e32 v41, v31
	v_mov_b32_e32 v30, v36
	v_mov_b32_e32 v31, v37
	v_mfma_f32_16x16x32_bf16 v[38:41], v[38:41], v[18:21], 0
	v_mov_b32_e32 v68, v44
	v_mov_b32_e32 v69, v45
	v_cvt_pk_f16_f32 v17, v0, v1
	v_pk_mul_f32 v[0:1], v[6:7], v[76:77]
	v_mfma_f32_16x16x32_bf16 v[34:37], v[72:75], v[22:25], v[38:41]
	v_cvt_f16_f32_e32 v10, v10
	v_cvt_f16_f32_e32 v11, v11
	v_cvt_f16_f32_e32 v12, v12
	v_pk_mul_f32 v[38:39], v[8:9], v[78:79]
	v_mfma_f32_16x16x32_bf16 v[6:9], v[30:33], v[18:21], 0
	v_cvt_f16_f32_e32 v13, v13
	v_cvt_f16_f32_e32 v20, v28
	v_cvt_f16_f32_e32 v21, v29
	v_mfma_f32_16x16x32_bf16 v[6:9], v[68:71], v[22:25], v[6:9]
	v_cndmask_b32_e64 v10, v10, 0, s[8:9]
	v_cndmask_b32_e64 v11, v11, 0, s[10:11]
	v_cvt_f16_f32_e32 v18, v26
	v_cvt_f16_f32_e32 v19, v27
	v_cndmask_b32_e64 v12, v12, 0, s[16:17]
	v_cndmask_b32_e64 v13, v13, 0, s[20:21]
	v_pack_b32_f16 v44, v10, v11
	v_cvt_f16_f32_e32 v10, v34
	v_cvt_f16_f32_e32 v11, v35
	v_cndmask_b32_e64 v20, v20, 0, s[4:5]
	v_cndmask_b32_e64 v21, v21, 0, s[6:7]
	v_pack_b32_f16 v45, v12, v13
	v_cvt_f16_f32_e32 v12, v36
	v_cvt_f16_f32_e32 v13, v37
	v_cvt_f16_f32_e32 v6, v6
	v_cvt_f16_f32_e32 v7, v7
	v_cvt_f16_f32_e32 v8, v8
	v_cvt_f16_f32_e32 v9, v9
	v_pack_b32_f16 v43, v20, v21
	v_lshl_or_b32 v20, v66, 14, v112
	v_add3_u32 v36, s3, v111, v20
	v_cndmask_b32_e64 v18, v18, 0, vcc
	v_cndmask_b32_e64 v19, 0, v19, s[0:1]
	v_cndmask_b32_e64 v10, v10, 0, s[12:13]
	v_cndmask_b32_e64 v11, v11, 0, s[14:15]
	v_add_u32_e32 v58, v36, v109
	v_add_u32_e32 v67, v36, v110
	v_cvt_pk_f16_f32 v0, v0, v1
	v_cvt_pk_f16_f32 v1, v38, v39
	v_pack_b32_f16 v42, v18, v19
	v_cndmask_b32_e64 v18, v12, 0, s[18:19]
	v_cndmask_b32_e64 v19, v13, 0, s[22:23]
	v_cndmask_b32_e64 v30, v6, 0, s[24:25]
	v_cndmask_b32_e64 v31, v7, 0, s[26:27]
	v_cndmask_b32_e64 v34, v8, 0, s[28:29]
	v_cndmask_b32_e64 v35, v9, 0, s[30:31]
	v_pack_b32_f16 v38, v10, v11
	ds_read2st64_b64 v[6:9], v58 offset1:4
	ds_read2st64_b64 v[10:13], v67 offset1:4
	v_add3_u32 v37, s33, v111, v20
	v_add_u32_e32 v96, v37, v109
	v_add_u32_e32 v97, v37, v110
	ds_read2st64_b64 v[22:25], v96 offset1:4
	ds_read2st64_b64 v[26:29], v97 offset1:4
	v_pack_b32_f16 v39, v18, v19
	s_waitcnt lgkmcnt(0)
	v_mov_b32_e32 v18, v6
	v_mov_b32_e32 v19, v7
	v_mov_b32_e32 v20, v10
	v_mov_b32_e32 v21, v11
	v_add_u32_e32 v98, v36, v107
	v_add_u32_e32 v99, v36, v108
	v_pack_b32_f16 v40, v30, v31
	v_mov_b32_e32 v30, v22
	v_mov_b32_e32 v31, v23
	v_mov_b32_e32 v32, v26
	v_mov_b32_e32 v33, v27
	ds_read2st64_b64 v[68:71], v98 offset1:4
	ds_read2st64_b64 v[72:75], v99 offset1:4
	v_mfma_f32_16x16x32_f16 v[18:21], v[18:21], v[42:45], 0
	v_mov_b32_e32 v10, v8
	v_mov_b32_e32 v11, v9
	v_add_u32_e32 v100, v37, v107
	v_add_u32_e32 v101, v37, v108
	ds_read2st64_b64 v[76:79], v100 offset1:4
	ds_read2st64_b64 v[80:83], v101 offset1:4
	v_mfma_f32_16x16x32_f16 v[18:21], v[30:33], v[14:17], v[18:21]
	s_waitcnt lgkmcnt(0)
	v_mov_b32_e32 v30, v68
	v_mov_b32_e32 v31, v69
	v_mov_b32_e32 v32, v72
	v_mov_b32_e32 v33, v73
	v_mov_b32_e32 v26, v24
	v_mov_b32_e32 v27, v25
	v_cvt_pk_f16_f32 v2, v2, v3
	v_cvt_pk_f16_f32 v3, v4, v5
	v_mfma_f32_16x16x32_f16 v[4:7], v[10:13], v[42:45], 0
	v_pack_b32_f16 v41, v34, v35
	v_mov_b32_e32 v34, v76
	v_mov_b32_e32 v35, v77
	v_mov_b32_e32 v36, v80
	v_mov_b32_e32 v37, v81
	v_mfma_f32_16x16x32_f16 v[18:21], v[30:33], v[38:41], v[18:21]
	v_mov_b32_e32 v72, v70
	v_mov_b32_e32 v73, v71
	v_mov_b32_e32 v80, v78
	v_mfma_f32_16x16x32_f16 v[4:7], v[26:29], v[14:17], v[4:7]
	v_mov_b32_e32 v81, v79
	s_mov_b32 s1, 0
	v_cmp_eq_u32_e32 vcc, 0, v104
	v_mfma_f32_16x16x32_f16 v[34:37], v[34:37], v[0:3], v[18:21]
	ds_read2st64_b64 v[8:11], v58 offset0:8 offset1:12
	s_nop 1
	ds_read2st64_b64 v[18:21], v67 offset0:8 offset1:12
	ds_read2st64_b64 v[22:25], v96 offset0:8 offset1:12
	ds_read2st64_b64 v[68:71], v97 offset0:8 offset1:12
	s_nop 1
	v_mul_f32_e32 v12, v35, v35
	v_mfma_f32_16x16x32_f16 v[4:7], v[72:75], v[38:41], v[4:7]
	s_waitcnt lgkmcnt(0)
	v_mov_b32_e32 v26, v22
	v_mov_b32_e32 v27, v23
	v_mov_b32_e32 v28, v68
	v_mfma_f32_16x16x32_f16 v[30:33], v[80:83], v[0:3], v[4:7]
	v_mov_b32_e32 v29, v69
	ds_read2st64_b64 v[72:75], v98 offset0:8 offset1:12
	ds_read2st64_b64 v[76:79], v99 offset0:8 offset1:12
	v_mov_b32_e32 v4, v8
	v_mov_b32_e32 v5, v9
	v_mov_b32_e32 v6, v18
	v_mov_b32_e32 v7, v19
	ds_read2st64_b64 v[80:83], v100 offset0:8 offset1:12
	ds_read2st64_b64 v[84:87], v101 offset0:8 offset1:12
	v_mfma_f32_16x16x32_f16 v[4:7], v[4:7], v[42:45], 0
	v_mov_b32_e32 v18, v10
	v_mov_b32_e32 v19, v11
	v_mov_b32_e32 v68, v24
	v_mfma_f32_16x16x32_f16 v[4:7], v[26:29], v[14:17], v[4:7]
	s_waitcnt lgkmcnt(0)
	v_mov_b32_e32 v26, v72
	v_mov_b32_e32 v27, v73
	v_mov_b32_e32 v28, v76
	v_mov_b32_e32 v29, v77
	v_mov_b32_e32 v69, v25
	v_mov_b32_e32 v76, v74
	v_mfma_f32_16x16x32_f16 v[4:7], v[26:29], v[38:41], v[4:7]
	v_mov_b32_e32 v26, v80
	v_mov_b32_e32 v27, v81
	v_mov_b32_e32 v28, v84
	v_mov_b32_e32 v29, v85
	v_mov_b32_e32 v77, v75
	v_mov_b32_e32 v84, v82
	v_mfma_f32_16x16x32_f16 v[26:29], v[26:29], v[0:3], v[4:7]
	v_mov_b32_e32 v85, v83
	v_mul_f32_e32 v13, v31, v31
	v_fmac_f32_e32 v12, v34, v34
	v_mfma_f32_16x16x32_f16 v[4:7], v[18:21], v[42:45], 0
	v_fmac_f32_e32 v13, v30, v30
	v_fmac_f32_e32 v12, v36, v36
	v_fmac_f32_e32 v13, v32, v32
	v_mfma_f32_16x16x32_f16 v[4:7], v[68:71], v[14:17], v[4:7]
	ds_read2st64_b64 v[8:11], v58 offset0:16 offset1:20
	ds_read2st64_b64 v[68:71], v67 offset0:16 offset1:20
	v_fmac_f32_e32 v12, v37, v37
	v_fmac_f32_e32 v13, v33, v33
	v_mfma_f32_16x16x32_f16 v[4:7], v[76:79], v[38:41], v[4:7]
	ds_read2st64_b64 v[72:75], v96 offset0:16 offset1:20
	ds_read2st64_b64 v[76:79], v97 offset0:16 offset1:20
	v_add_f32_e32 v12, v12, v13
	v_mul_f32_e32 v13, v27, v27
	v_mfma_f32_16x16x32_f16 v[22:25], v[84:87], v[0:3], v[4:7]
	s_waitcnt lgkmcnt(0)
	v_mov_b32_e32 v18, v72
	v_mov_b32_e32 v19, v73
	v_mov_b32_e32 v20, v76
	v_mov_b32_e32 v4, v8
	v_mov_b32_e32 v5, v9
	v_mov_b32_e32 v6, v68
	v_mov_b32_e32 v7, v69
	v_mov_b32_e32 v21, v77
	ds_read2st64_b64 v[80:83], v98 offset0:16 offset1:20
	ds_read2st64_b64 v[84:87], v99 offset0:16 offset1:20
	v_mfma_f32_16x16x32_f16 v[4:7], v[4:7], v[42:45], 0
	ds_read2st64_b64 v[88:91], v100 offset0:16 offset1:20
	ds_read2st64_b64 v[92:95], v101 offset0:16 offset1:20
	v_mov_b32_e32 v68, v10
	v_mov_b32_e32 v69, v11
	v_mfma_f32_16x16x32_f16 v[4:7], v[18:21], v[14:17], v[4:7]
	s_waitcnt lgkmcnt(0)
	v_mov_b32_e32 v18, v80
	v_mov_b32_e32 v19, v81
	v_mov_b32_e32 v20, v84
	v_mov_b32_e32 v21, v85
	v_mov_b32_e32 v76, v74
	v_mov_b32_e32 v77, v75
	v_mfma_f32_16x16x32_f16 v[4:7], v[18:21], v[38:41], v[4:7]
	v_mov_b32_e32 v18, v88
	v_mov_b32_e32 v19, v89
	v_mov_b32_e32 v20, v92
	v_mov_b32_e32 v21, v93
	v_mov_b32_e32 v84, v82
	v_mov_b32_e32 v85, v83
	v_mfma_f32_16x16x32_f16 v[18:21], v[18:21], v[0:3], v[4:7]
	v_mov_b32_e32 v92, v90
	v_mov_b32_e32 v93, v91
	v_fmac_f32_e32 v13, v26, v26
	v_mfma_f32_16x16x32_f16 v[4:7], v[68:71], v[42:45], 0
	ds_read2st64_b64 v[68:71], v58 offset0:24 offset1:28
	ds_read2st64_b64 v[72:75], v67 offset0:24 offset1:28
	v_fmac_f32_e32 v13, v28, v28
	v_fmac_f32_e32 v13, v29, v29
	v_mfma_f32_16x16x32_f16 v[4:7], v[76:79], v[14:17], v[4:7]
	ds_read2st64_b64 v[76:79], v96 offset0:24 offset1:28
	ds_read2st64_b64 v[80:83], v97 offset0:24 offset1:28
	v_add_f32_e32 v12, v12, v13
	v_mul_f32_e32 v13, v23, v23
	v_mfma_f32_16x16x32_f16 v[4:7], v[84:87], v[38:41], v[4:7]
	v_fmac_f32_e32 v13, v22, v22
	v_fmac_f32_e32 v13, v24, v24
	v_fmac_f32_e32 v13, v25, v25
	v_mfma_f32_16x16x32_f16 v[8:11], v[92:95], v[0:3], v[4:7]
	s_waitcnt lgkmcnt(0)
	v_mov_b32_e32 v84, v76
	v_mov_b32_e32 v85, v77
	v_mov_b32_e32 v86, v80
	v_mov_b32_e32 v4, v68
	v_mov_b32_e32 v5, v69
	v_mov_b32_e32 v6, v72
	v_mov_b32_e32 v7, v73
	v_mov_b32_e32 v72, v70
	v_mov_b32_e32 v73, v71
	v_mov_b32_e32 v87, v81
	ds_read2st64_b64 v[88:91], v98 offset0:24 offset1:28
	ds_read2st64_b64 v[92:95], v99 offset0:24 offset1:28
	v_add_f32_e32 v12, v12, v13
	v_mul_f32_e32 v13, v19, v19
	v_mfma_f32_16x16x32_f16 v[4:7], v[4:7], v[42:45], 0
	v_fmac_f32_e32 v13, v18, v18
	v_fmac_f32_e32 v13, v20, v20
	v_mov_b32_e32 v80, v78
	v_mov_b32_e32 v81, v79
	v_fmac_f32_e32 v13, v21, v21
	v_mfma_f32_16x16x32_f16 v[42:45], v[72:75], v[42:45], 0
	v_add_f32_e32 v12, v12, v13
	v_mul_f32_e32 v13, v9, v9
	ds_read2st64_b64 v[96:99], v100 offset0:24 offset1:28
	ds_read2st64_b64 v[108:111], v101 offset0:24 offset1:28
	v_mfma_f32_16x16x32_f16 v[4:7], v[84:87], v[14:17], v[4:7]
	s_waitcnt lgkmcnt(0)
	v_mov_b32_e32 v84, v88
	v_mov_b32_e32 v85, v89
	v_mov_b32_e32 v86, v92
	v_mov_b32_e32 v87, v93
	v_fmac_f32_e32 v13, v8, v8
	v_fmac_f32_e32 v13, v10, v10
	v_fmac_f32_e32 v13, v11, v11
	v_mov_b32_e32 v92, v90
	v_mov_b32_e32 v93, v91
	v_add_f32_e32 v58, v12, v13
	v_mfma_f32_16x16x32_f16 v[12:15], v[80:83], v[14:17], v[42:45]
	v_mfma_f32_16x16x32_f16 v[4:7], v[84:87], v[38:41], v[4:7]
	v_mov_b32_e32 v84, v96
	v_mov_b32_e32 v85, v97
	v_mov_b32_e32 v86, v108
	v_mov_b32_e32 v87, v109
	v_mov_b32_e32 v108, v98
	v_mov_b32_e32 v109, v99
	v_mfma_f32_16x16x32_f16 v[12:15], v[92:95], v[38:41], v[12:15]
	v_mfma_f32_16x16x32_f16 v[4:7], v[84:87], v[0:3], v[4:7]
	v_mfma_f32_16x16x32_f16 v[0:3], v[108:111], v[0:3], v[12:15]
	s_nop 5
	v_and_b32_e32 v14, 0x70, v105
	v_mul_f32_e32 v67, v5, v5
	v_fmac_f32_e32 v67, v4, v4
	v_mul_f32_e32 v12, v1, v1
	v_fmac_f32_e32 v67, v6, v6
	v_fmac_f32_e32 v12, v0, v0
	v_fmac_f32_e32 v67, v7, v7
	v_fmac_f32_e32 v12, v2, v2
	v_add_f32_e32 v16, v58, v67
	v_fmac_f32_e32 v12, v3, v3
	v_add_f32_e32 v12, v16, v12
	ds_bpermute_b32 v13, v64, v12
	s_waitcnt lgkmcnt(0)
	v_add_f32_e32 v12, v12, v13
	ds_bpermute_b32 v15, v65, v12
	v_lshlrev_b32_e32 v13, 7, v66
	s_waitcnt lgkmcnt(0)
	v_add_f32_e32 v12, v12, v15
	s_and_saveexec_b64 s[4:5], vcc
	v_lshlrev_b32_e32 v15, 2, v14
	s_add_i32 s0, 0, 0x26600
	v_lshlrev_b32_e32 v16, 2, v103
	v_add3_u32 v15, s0, v15, v16
	ds_write_b32 v15, v12
	s_or_b64 exec, exec, s[4:5]
	v_bitop3_b32 v14, v14, 64, v103 bitop3:0x36
	v_lshl_add_u32 v14, v14, 2, 0
	v_add_u32_e32 v14, 0x26600, v14
	s_waitcnt vmcnt(0) lgkmcnt(0)
	s_barrier
	ds_read_b32 v38, v14
	v_cvt_f32_f16_e32 v40, v62
	s_mov_b32 s4, 0x800000
	v_or_b32_e32 v13, v13, v106
	v_lshl_add_u32 v14, v13, 2, 0
	s_waitcnt lgkmcnt(0)
	v_add_f32_e32 v12, v12, v38
	v_mov_b32_e32 v38, 0x3727c5ac
	v_fmac_f32_e32 v38, 0x33800000, v12
	v_mul_f32_e32 v12, 0x4b800000, v38
	v_cmp_gt_f32_e32 vcc, s4, v38
	v_mul_f32_e32 v41, 0xbfb8aa3b, v40
	v_exp_f32_e32 v42, v41
	v_cndmask_b32_e32 v12, v38, v12, vcc
	v_cvt_f32_f16_sdwa v41, v62 dst_sel:DWORD dst_unused:UNUSED_PAD src0_sel:WORD_1
	v_rsq_f32_e32 v12, v12
	v_add_u32_e32 v44, 0x26200, v14
	ds_read_b128 v[14:17], v44
	v_mul_f32_e32 v43, 0xbfb8aa3b, v41
	v_mul_f32_e32 v38, 0x45800000, v12
	v_exp_f32_e32 v43, v43
	v_cndmask_b32_e32 v12, v12, v38, vcc
	v_mul_f32_e32 v12, 0x3b800000, v12
	v_pk_mul_f32 v[34:35], v[12:13], v[34:35] op_sel_hi:[0,1]
	s_waitcnt lgkmcnt(0)
	v_pk_mul_f32 v[14:15], v[14:15], v[34:35]
	v_add_f32_e32 v34, 1.0, v43
	v_rcp_f32_e32 v43, v34
	v_cvt_f32_f16_e32 v34, v63
	v_add_f32_e32 v42, 1.0, v42
	v_cvt_f32_f16_sdwa v35, v63 dst_sel:DWORD dst_unused:UNUSED_PAD src0_sel:WORD_1
	v_rcp_f32_e32 v42, v42
	v_pk_mul_f32 v[14:15], v[14:15], v[40:41]
	v_mul_f32_e32 v40, 0xbfb8aa3b, v34
	v_exp_f32_e32 v41, v40
	v_mul_f32_e32 v40, 0xbfb8aa3b, v35
	v_pk_mul_f32 v[14:15], v[14:15], v[42:43]
	v_exp_f32_e32 v42, v40
	v_cvt_pk_f16_f32 v40, v14, v15
	v_add_f32_e32 v14, 1.0, v41
	v_rcp_f32_e32 v14, v14
	v_add_f32_e32 v15, 1.0, v42
	v_rcp_f32_e32 v15, v15
	s_lshl_b32 s0, s2, 4
	s_lshl_b32 s2, s2, 6
	v_pk_mul_f32 v[36:37], v[12:13], v[36:37] op_sel_hi:[0,1]
	s_and_b32 s3, s0, 0xfffff800
	s_and_b32 s2, s2, 0x7c0
	v_pk_mul_f32 v[16:17], v[16:17], v[36:37]
	s_or_b32 s2, s3, s2
	v_pk_mul_f32 v[16:17], v[16:17], v[34:35]
	v_or_b32_e32 v38, s2, v102
	v_pk_mul_f32 v[14:15], v[16:17], v[14:15]
	v_cvt_f32_f16_e32 v16, v60
	v_ashrrev_i32_e32 v39, 31, v38
	v_cvt_f32_f16_sdwa v17, v60 dst_sel:DWORD dst_unused:UNUSED_PAD src0_sel:WORD_1
	v_lshlrev_b64 v[38:39], 11, v[38:39]
	v_lshl_add_u64 v[38:39], s[42:43], 0, v[38:39]
	s_and_b32 s0, s0, 0x600
	v_lshl_add_u64 v[38:39], v[38:39], 0, s[0:1]
	v_lshlrev_b32_e32 v58, 1, v13
	v_mul_f32_e32 v13, 0xbfb8aa3b, v16
	v_cvt_pk_f16_f32 v41, v14, v15
	v_lshl_add_u64 v[14:15], v[38:39], 0, v[58:59]
	v_exp_f32_e32 v13, v13
	v_mul_f32_e32 v38, 0xbfb8aa3b, v17
	ds_read_b128 v[34:37], v44 offset:64
	v_exp_f32_e32 v38, v38
	v_add_f32_e32 v13, 1.0, v13
	v_rcp_f32_e32 v42, v13
	v_pk_mul_f32 v[30:31], v[12:13], v[30:31] op_sel_hi:[0,1]
	v_add_f32_e32 v13, 1.0, v38
	global_store_dwordx2 v[14:15], v[40:41], off
	v_rcp_f32_e32 v43, v13
	ds_read_b128 v[38:41], v44 offset:128
	s_waitcnt lgkmcnt(1)
	v_pk_mul_f32 v[30:31], v[34:35], v[30:31]
	v_cvt_f32_f16_e32 v34, v61
	v_cvt_f32_f16_sdwa v35, v61 dst_sel:DWORD dst_unused:UNUSED_PAD src0_sel:WORD_1
	v_pk_mul_f32 v[16:17], v[30:31], v[16:17]
	v_mul_f32_e32 v13, 0xbfb8aa3b, v34
	v_pk_mul_f32 v[16:17], v[16:17], v[42:43]
	v_exp_f32_e32 v13, v13
	v_cvt_pk_f16_f32 v16, v16, v17
	v_mul_f32_e32 v17, 0xbfb8aa3b, v35
	v_exp_f32_e32 v17, v17
	v_add_f32_e32 v13, 1.0, v13
	v_rcp_f32_e32 v30, v13
	v_pk_mul_f32 v[32:33], v[12:13], v[32:33] op_sel_hi:[0,1]
	v_add_f32_e32 v13, 1.0, v17
	v_rcp_f32_e32 v31, v13
	v_cvt_f32_f16_e32 v42, v56
	v_pk_mul_f32 v[32:33], v[36:37], v[32:33]
	v_cvt_f32_f16_sdwa v43, v56 dst_sel:DWORD dst_unused:UNUSED_PAD src0_sel:WORD_1
	v_pk_mul_f32 v[32:33], v[32:33], v[34:35]
	v_mul_f32_e32 v13, 0xbfb8aa3b, v42
	v_pk_mul_f32 v[30:31], v[32:33], v[30:31]
	v_exp_f32_e32 v13, v13
	v_cvt_pk_f16_f32 v17, v30, v31
	global_store_dwordx2 v[14:15], v[16:17], off offset:32
	v_mul_f32_e32 v16, 0xbfb8aa3b, v43
	v_exp_f32_e32 v17, v16
	v_add_f32_e32 v13, 1.0, v13
	v_rcp_f32_e32 v16, v13
	v_pk_mul_f32 v[26:27], v[12:13], v[26:27] op_sel_hi:[0,1]
	v_add_f32_e32 v13, 1.0, v17
	v_cvt_f32_f16_e32 v30, v57
	v_rcp_f32_e32 v17, v13
	v_cvt_f32_f16_sdwa v31, v57 dst_sel:DWORD dst_unused:UNUSED_PAD src0_sel:WORD_1
	s_waitcnt lgkmcnt(0)
	v_pk_mul_f32 v[26:27], v[38:39], v[26:27]
	v_mul_f32_e32 v13, 0xbfb8aa3b, v30
	v_pk_mul_f32 v[26:27], v[26:27], v[42:43]
	v_exp_f32_e32 v13, v13
	v_pk_mul_f32 v[16:17], v[26:27], v[16:17]
	v_mul_f32_e32 v26, 0xbfb8aa3b, v31
	v_exp_f32_e32 v27, v26
	v_add_f32_e32 v13, 1.0, v13
	v_rcp_f32_e32 v26, v13
	v_cvt_f32_f16_e32 v34, v52
	v_add_f32_e32 v13, 1.0, v27
	v_rcp_f32_e32 v27, v13
	v_pk_mul_f32 v[28:29], v[12:13], v[28:29] op_sel_hi:[0,1]
	v_pk_mul_f32 v[28:29], v[40:41], v[28:29]
	v_cvt_f32_f16_sdwa v35, v52 dst_sel:DWORD dst_unused:UNUSED_PAD src0_sel:WORD_1
	v_pk_mul_f32 v[28:29], v[28:29], v[30:31]
	v_cvt_pk_f16_f32 v16, v16, v17
	v_pk_mul_f32 v[26:27], v[28:29], v[26:27]
	v_mul_f32_e32 v13, 0xbfb8aa3b, v34
	v_cvt_pk_f16_f32 v17, v26, v27
	global_store_dwordx2 v[14:15], v[16:17], off offset:64
	v_exp_f32_e32 v13, v13
	v_mul_f32_e32 v16, 0xbfb8aa3b, v35
	ds_read_b128 v[26:29], v44 offset:192
	ds_read_b128 v[30:33], v44 offset:256
	v_exp_f32_e32 v17, v16
	v_add_f32_e32 v13, 1.0, v13
	v_rcp_f32_e32 v16, v13
	v_pk_mul_f32 v[22:23], v[12:13], v[22:23] op_sel_hi:[0,1]
	v_add_f32_e32 v13, 1.0, v17
	v_rcp_f32_e32 v17, v13
	s_waitcnt lgkmcnt(1)
	v_pk_mul_f32 v[22:23], v[26:27], v[22:23]
	v_cvt_f32_f16_e32 v26, v53
	v_cvt_f32_f16_sdwa v27, v53 dst_sel:DWORD dst_unused:UNUSED_PAD src0_sel:WORD_1
	v_pk_mul_f32 v[22:23], v[22:23], v[34:35]
	v_cvt_f32_f16_e32 v34, v54
	v_pk_mul_f32 v[16:17], v[22:23], v[16:17]
	v_mul_f32_e32 v13, 0xbfb8aa3b, v26
	v_exp_f32_e32 v13, v13
	v_cvt_pk_f16_f32 v16, v16, v17
	v_mul_f32_e32 v17, 0xbfb8aa3b, v27
	v_exp_f32_e32 v17, v17
	v_add_f32_e32 v13, 1.0, v13
	v_rcp_f32_e32 v22, v13
	v_pk_mul_f32 v[24:25], v[12:13], v[24:25] op_sel_hi:[0,1]
	v_add_f32_e32 v13, 1.0, v17
	v_rcp_f32_e32 v23, v13
	v_pk_mul_f32 v[24:25], v[28:29], v[24:25]
	v_cvt_f32_f16_sdwa v35, v54 dst_sel:DWORD dst_unused:UNUSED_PAD src0_sel:WORD_1
	v_pk_mul_f32 v[24:25], v[24:25], v[26:27]
	v_mul_f32_e32 v13, 0xbfb8aa3b, v34
	v_pk_mul_f32 v[22:23], v[24:25], v[22:23]
	v_exp_f32_e32 v13, v13
	v_cvt_pk_f16_f32 v17, v22, v23
	global_store_dwordx2 v[14:15], v[16:17], off offset:96
	v_mul_f32_e32 v16, 0xbfb8aa3b, v35
	v_exp_f32_e32 v17, v16
	v_add_f32_e32 v13, 1.0, v13
	v_rcp_f32_e32 v16, v13
	v_pk_mul_f32 v[18:19], v[12:13], v[18:19] op_sel_hi:[0,1]
	v_add_f32_e32 v13, 1.0, v17
	v_cvt_f32_f16_e32 v22, v55
	v_rcp_f32_e32 v17, v13
	v_cvt_f32_f16_sdwa v23, v55 dst_sel:DWORD dst_unused:UNUSED_PAD src0_sel:WORD_1
	s_waitcnt lgkmcnt(0)
	v_pk_mul_f32 v[18:19], v[30:31], v[18:19]
	v_mul_f32_e32 v13, 0xbfb8aa3b, v22
	v_pk_mul_f32 v[18:19], v[18:19], v[34:35]
	v_exp_f32_e32 v13, v13
	v_pk_mul_f32 v[16:17], v[18:19], v[16:17]
	v_mul_f32_e32 v18, 0xbfb8aa3b, v23
	v_exp_f32_e32 v19, v18
	v_add_f32_e32 v13, 1.0, v13
	v_rcp_f32_e32 v18, v13
	v_cvt_f32_f16_e32 v24, v50
	v_add_f32_e32 v13, 1.0, v19
	v_rcp_f32_e32 v19, v13
	v_cvt_f32_f16_sdwa v25, v50 dst_sel:DWORD dst_unused:UNUSED_PAD src0_sel:WORD_1
	v_pk_mul_f32 v[20:21], v[12:13], v[20:21] op_sel_hi:[0,1]
	v_pk_mul_f32 v[20:21], v[32:33], v[20:21]
	v_mul_f32_e32 v13, 0xbfb8aa3b, v24
	v_pk_mul_f32 v[20:21], v[20:21], v[22:23]
	v_exp_f32_e32 v13, v13
	v_pk_mul_f32 v[18:19], v[20:21], v[18:19]
	v_mul_f32_e32 v20, 0xbfb8aa3b, v25
	v_cvt_pk_f16_f32 v16, v16, v17
	v_cvt_pk_f16_f32 v17, v18, v19
	v_exp_f32_e32 v20, v20
	global_store_dwordx2 v[14:15], v[16:17], off offset:128
	ds_read_b128 v[16:19], v44 offset:320
	v_add_f32_e32 v13, 1.0, v13
	v_rcp_f32_e32 v26, v13
	v_pk_mul_f32 v[8:9], v[12:13], v[8:9] op_sel_hi:[0,1]
	v_add_f32_e32 v13, 1.0, v20
	v_rcp_f32_e32 v27, v13
	ds_read_b128 v[20:23], v44 offset:384
	s_waitcnt lgkmcnt(1)
	v_pk_mul_f32 v[8:9], v[16:17], v[8:9]
	v_cvt_f32_f16_e32 v16, v51
	v_cvt_f32_f16_sdwa v17, v51 dst_sel:DWORD dst_unused:UNUSED_PAD src0_sel:WORD_1
	v_pk_mul_f32 v[8:9], v[8:9], v[24:25]
	v_mul_f32_e32 v13, 0xbfb8aa3b, v16
	v_pk_mul_f32 v[8:9], v[8:9], v[26:27]
	v_exp_f32_e32 v13, v13
	v_cvt_pk_f16_f32 v8, v8, v9
	v_mul_f32_e32 v9, 0xbfb8aa3b, v17
	v_exp_f32_e32 v9, v9
	v_add_f32_e32 v13, 1.0, v13
	v_rcp_f32_e32 v24, v13
	v_pk_mul_f32 v[10:11], v[12:13], v[10:11] op_sel_hi:[0,1]
	v_add_f32_e32 v9, 1.0, v9
	v_rcp_f32_e32 v25, v9
	v_pk_mul_f32 v[10:11], v[18:19], v[10:11]
	v_pk_mul_f32 v[4:5], v[12:13], v[4:5] op_sel_hi:[0,1]
	v_pk_mul_f32 v[10:11], v[10:11], v[16:17]
	v_cvt_f32_f16_e32 v16, v48
	v_cvt_f32_f16_sdwa v17, v48 dst_sel:DWORD dst_unused:UNUSED_PAD src0_sel:WORD_1
	v_pk_mul_f32 v[10:11], v[10:11], v[24:25]
	s_waitcnt lgkmcnt(0)
	v_pk_mul_f32 v[4:5], v[20:21], v[4:5]
	v_cvt_pk_f16_f32 v9, v10, v11
	v_mul_f32_e32 v10, 0xbfb8aa3b, v16
	global_store_dwordx2 v[14:15], v[8:9], off offset:160
	v_mul_f32_e32 v8, 0xbfb8aa3b, v17
	v_exp_f32_e32 v10, v10
	v_exp_f32_e32 v9, v8
	v_cvt_f32_f16_sdwa v11, v49 dst_sel:DWORD dst_unused:UNUSED_PAD src0_sel:WORD_1
	v_pk_mul_f32 v[4:5], v[4:5], v[16:17]
	v_add_f32_e32 v8, 1.0, v10
	v_add_f32_e32 v9, 1.0, v9
	v_rcp_f32_e32 v8, v8
	v_rcp_f32_e32 v9, v9
	v_cvt_f32_f16_e32 v10, v49
	v_pk_mul_f32 v[6:7], v[12:13], v[6:7] op_sel_hi:[0,1]
	v_cvt_f32_f16_e32 v16, v46
	v_pk_mul_f32 v[4:5], v[4:5], v[8:9]
	v_mul_f32_e32 v8, 0xbfb8aa3b, v10
	v_cvt_pk_f16_f32 v4, v4, v5
	v_mul_f32_e32 v5, 0xbfb8aa3b, v11
	v_exp_f32_e32 v8, v8
	v_exp_f32_e32 v5, v5
	v_pk_mul_f32 v[6:7], v[22:23], v[6:7]
	v_cvt_f32_f16_sdwa v17, v46 dst_sel:DWORD dst_unused:UNUSED_PAD src0_sel:WORD_1
	v_add_f32_e32 v8, 1.0, v8
	v_add_f32_e32 v5, 1.0, v5
	v_rcp_f32_e32 v8, v8
	v_rcp_f32_e32 v9, v5
	v_pk_mul_f32 v[6:7], v[6:7], v[10:11]
	v_pk_mul_f32 v[0:1], v[12:13], v[0:1] op_sel_hi:[0,1]
	v_pk_mul_f32 v[2:3], v[12:13], v[2:3] op_sel_hi:[0,1]
	v_pk_mul_f32 v[6:7], v[6:7], v[8:9]
	v_mul_f32_e32 v9, 0xbfb8aa3b, v17
	v_cvt_pk_f16_f32 v5, v6, v7
	v_mul_f32_e32 v6, 0xbfb8aa3b, v16
	v_exp_f32_e32 v8, v6
	global_store_dwordx2 v[14:15], v[4:5], off offset:192
	ds_read_b128 v[4:7], v44 offset:448
	v_exp_f32_e32 v9, v9
	v_add_f32_e32 v8, 1.0, v8
	v_rcp_f32_e32 v8, v8
	s_waitcnt lgkmcnt(0)
	v_pk_mul_f32 v[0:1], v[4:5], v[0:1]
	v_add_f32_e32 v4, 1.0, v9
	v_rcp_f32_e32 v9, v4
	v_cvt_f32_f16_e32 v4, v47
	v_cvt_f32_f16_sdwa v5, v47 dst_sel:DWORD dst_unused:UNUSED_PAD src0_sel:WORD_1
	v_pk_mul_f32 v[0:1], v[0:1], v[16:17]
	v_pk_mul_f32 v[2:3], v[6:7], v[2:3]
	v_pk_mul_f32 v[0:1], v[0:1], v[8:9]
	v_mul_f32_e32 v8, 0xbfb8aa3b, v4
	v_exp_f32_e32 v8, v8
	v_mul_f32_e32 v9, 0xbfb8aa3b, v5
	v_exp_f32_e32 v9, v9
	v_cvt_pk_f16_f32 v0, v0, v1
	v_add_f32_e32 v1, 1.0, v8
	v_rcp_f32_e32 v8, v1
	v_add_f32_e32 v1, 1.0, v9
	v_rcp_f32_e32 v9, v1
	v_pk_mul_f32 v[2:3], v[2:3], v[4:5]
	s_nop 0
	v_pk_mul_f32 v[2:3], v[2:3], v[8:9]
	s_nop 0
	v_cvt_pk_f16_f32 v1, v2, v3
	global_store_dwordx2 v[14:15], v[0:1], off offset:224
	s_endpgm

	.amdhsa_kernel _Z9attn_fastPKtS0_S0_S0_S0_S0_S0_S0_S0_PKfS2_Pt
		.amdhsa_group_segment_fixed_size 0
		.amdhsa_private_segment_fixed_size 0
		.amdhsa_kernarg_size 96
		.amdhsa_user_sgpr_count 2
		.amdhsa_user_sgpr_dispatch_ptr 0
		.amdhsa_user_sgpr_queue_ptr 0
		.amdhsa_user_sgpr_kernarg_segment_ptr 1
		.amdhsa_user_sgpr_dispatch_id 0
		.amdhsa_user_sgpr_kernarg_preload_length 0
		.amdhsa_user_sgpr_kernarg_preload_offset 0
		.amdhsa_user_sgpr_private_segment_size 0
		.amdhsa_uses_dynamic_stack 0
		.amdhsa_enable_private_segment 0
		.amdhsa_system_sgpr_workgroup_id_x 1
		.amdhsa_system_sgpr_workgroup_id_y 0
		.amdhsa_system_sgpr_workgroup_id_z 0
		.amdhsa_system_sgpr_workgroup_info 0
		.amdhsa_system_vgpr_workitem_id 0
		.amdhsa_next_free_vgpr 156
		.amdhsa_next_free_sgpr 46
		.amdhsa_accum_offset 156
		.amdhsa_reserve_vcc 1
		.amdhsa_float_round_mode_32 0
		.amdhsa_float_round_mode_16_64 0
		.amdhsa_float_denorm_mode_32 3
		.amdhsa_float_denorm_mode_16_64 3
		.amdhsa_dx10_clamp 1
		.amdhsa_ieee_mode 1
		.amdhsa_fp16_overflow 0
		.amdhsa_tg_split 0
		.amdhsa_exception_fp_ieee_invalid_op 0
		.amdhsa_exception_fp_denorm_src 0
		.amdhsa_exception_fp_ieee_div_zero 0
		.amdhsa_exception_fp_ieee_overflow 0
		.amdhsa_exception_fp_ieee_underflow 0
		.amdhsa_exception_fp_ieee_inexact 0
		.amdhsa_exception_int_div_zero 0
	.end_amdhsa_kernel

amdhsa.kernels:
  - .agpr_count:     0
    .args:
      - .actual_access:  read_only
        .address_space:  global
        .offset:         0
        .size:           8
        .value_kind:     global_buffer
      - .actual_access:  read_only
        .address_space:  global
        .offset:         8
        .size:           8
        .value_kind:     global_buffer
      - .actual_access:  write_only
        .address_space:  global
        .offset:         16
        .size:           8
        .value_kind:     global_buffer
      - .offset:         24
        .size:           4
        .value_kind:     by_value
      - .offset:         28
        .size:           4
        .value_kind:     by_value
      - .offset:         32
        .size:           4
        .value_kind:     by_value
      - .offset:         36
        .size:           4
        .value_kind:     by_value
    .group_segment_fixed_size: 8256
    .kernarg_segment_align: 8
    .kernarg_segment_size: 40
    .language:       OpenCL C
    .language_version:
      - 2
      - 0
    .max_flat_workgroup_size: 256
    .name:           _Z14gemm_f32_naivePKfS0_Pfiiii
    .private_segment_fixed_size: 0
    .sgpr_count:     24
    .sgpr_spill_count: 0
    .symbol:         _Z14gemm_f32_naivePKfS0_Pfiiii.kd
    .uniform_work_group_size: 1
    .uses_dynamic_stack: false
    .vgpr_count:     76
    .vgpr_spill_count: 0
    .wavefront_size: 64
  - .agpr_count:     0
    .args:
      - .actual_access:  read_only
        .address_space:  global
        .offset:         0
        .size:           8
        .value_kind:     global_buffer
      - .actual_access:  write_only
        .address_space:  global
        .offset:         8
        .size:           8
        .value_kind:     global_buffer
      - .actual_access:  write_only
        .address_space:  global
        .offset:         16
        .size:           8
        .value_kind:     global_buffer
      - .actual_access:  write_only
        .address_space:  global
        .offset:         24
        .size:           8
        .value_kind:     global_buffer
      - .actual_access:  write_only
        .address_space:  global
        .offset:         32
        .size:           8
        .value_kind:     global_buffer
      - .actual_access:  write_only
        .address_space:  global
        .offset:         40
        .size:           8
        .value_kind:     global_buffer
      - .actual_access:  write_only
        .address_space:  global
        .offset:         48
        .size:           8
        .value_kind:     global_buffer
    .group_segment_fixed_size: 0
    .kernarg_segment_align: 8
    .kernarg_segment_size: 56
    .language:       OpenCL C
    .language_version:
      - 2
      - 0
    .max_flat_workgroup_size: 256
    .name:           _Z10post_naivePKfPtS1_S1_S1_S1_S1_
    .private_segment_fixed_size: 0
    .sgpr_count:     28
    .sgpr_spill_count: 0
    .symbol:         _Z10post_naivePKfPtS1_S1_S1_S1_S1_.kd
    .uniform_work_group_size: 1
    .uses_dynamic_stack: false
    .vgpr_count:     38
    .vgpr_spill_count: 0
    .wavefront_size: 64
  - .agpr_count:     0
    .args:
      - .actual_access:  read_only
        .address_space:  global
        .offset:         0
        .size:           8
        .value_kind:     global_buffer
      - .actual_access:  read_only
        .address_space:  global
        .offset:         8
        .size:           8
        .value_kind:     global_buffer
      - .actual_access:  read_only
        .address_space:  global
        .offset:         16
        .size:           8
        .value_kind:     global_buffer
      - .actual_access:  read_only
        .address_space:  global
        .offset:         24
        .size:           8
        .value_kind:     global_buffer
      - .actual_access:  read_only
        .address_space:  global
        .offset:         32
        .size:           8
        .value_kind:     global_buffer
      - .actual_access:  read_only
        .address_space:  global
        .offset:         40
        .size:           8
        .value_kind:     global_buffer
      - .actual_access:  read_only
        .address_space:  global
        .offset:         48
        .size:           8
        .value_kind:     global_buffer
      - .actual_access:  write_only
        .address_space:  global
        .offset:         56
        .size:           8
        .value_kind:     global_buffer
      - .actual_access:  write_only
        .address_space:  global
        .offset:         64
        .size:           8
        .value_kind:     global_buffer
      - .actual_access:  write_only
        .address_space:  global
        .offset:         72
        .size:           8
        .value_kind:     global_buffer
      - .actual_access:  write_only
        .address_space:  global
        .offset:         80
        .size:           8
        .value_kind:     global_buffer
    .group_segment_fixed_size: 1152
    .kernarg_segment_align: 8
    .kernarg_segment_size: 88
    .language:       OpenCL C
    .language_version:
      - 2
      - 0
    .max_flat_workgroup_size: 256
    .name:           _Z11gates_naivePKfS0_S0_S0_S0_S0_S0_PtS1_S1_S1_
    .private_segment_fixed_size: 0
    .sgpr_count:     32
    .sgpr_spill_count: 0
    .symbol:         _Z11gates_naivePKfS0_S0_S0_S0_S0_S0_PtS1_S1_S1_.kd
    .uniform_work_group_size: 1
    .uses_dynamic_stack: false
    .vgpr_count:     66
    .vgpr_spill_count: 0
    .wavefront_size: 64
  - .agpr_count:     0
    .args:
      - .actual_access:  read_only
        .address_space:  global
        .offset:         0
        .size:           8
        .value_kind:     global_buffer
      - .actual_access:  read_only
        .address_space:  global
        .offset:         8
        .size:           8
        .value_kind:     global_buffer
      - .actual_access:  read_only
        .address_space:  global
        .offset:         16
        .size:           8
        .value_kind:     global_buffer
      - .actual_access:  read_only
        .address_space:  global
        .offset:         24
        .size:           8
        .value_kind:     global_buffer
      - .actual_access:  read_only
        .address_space:  global
        .offset:         32
        .size:           8
        .value_kind:     global_buffer
      - .actual_access:  read_only
        .address_space:  global
        .offset:         40
        .size:           8
        .value_kind:     global_buffer
      - .actual_access:  read_only
        .address_space:  global
        .offset:         48
        .size:           8
        .value_kind:     global_buffer
      - .actual_access:  write_only
        .address_space:  global
        .offset:         56
        .size:           8
        .value_kind:     global_buffer
    .group_segment_fixed_size: 12560
    .kernarg_segment_align: 8
    .kernarg_segment_size: 64
    .language:       OpenCL C
    .language_version:
      - 2
      - 0
    .max_flat_workgroup_size: 256
    .name:           _Z10attn_naivePKtS0_S0_S0_S0_S0_PKfPf
    .private_segment_fixed_size: 0
    .sgpr_count:     33
    .sgpr_spill_count: 0
    .symbol:         _Z10attn_naivePKtS0_S0_S0_S0_S0_PKfPf.kd
    .uniform_work_group_size: 1
    .uses_dynamic_stack: false
    .vgpr_count:     82
    .vgpr_spill_count: 0
    .wavefront_size: 64
  - .agpr_count:     0
    .args:
      - .address_space:  global
        .offset:         0
        .size:           8
        .value_kind:     global_buffer
      - .address_space:  global
        .offset:         8
        .size:           8
        .value_kind:     global_buffer
      - .actual_access:  write_only
        .address_space:  global
        .offset:         16
        .size:           8
        .value_kind:     global_buffer
    .group_segment_fixed_size: 0
    .kernarg_segment_align: 8
    .kernarg_segment_size: 24
    .language:       OpenCL C
    .language_version:
      - 2
      - 0
    .max_flat_workgroup_size: 512
    .name:           _Z8gemm_outPKtS0_Pf
    .private_segment_fixed_size: 0
    .sgpr_count:     26
    .sgpr_spill_count: 0
    .symbol:         _Z8gemm_outPKtS0_Pf.kd
    .uniform_work_group_size: 1
    .uses_dynamic_stack: false
    .vgpr_count:     158
    .vgpr_spill_count: 0
    .wavefront_size: 64
  - .agpr_count:     0
    .args:
      - .address_space:  global
        .offset:         0
        .size:           8
        .value_kind:     global_buffer
      - .address_space:  global
        .offset:         8
        .size:           8
        .value_kind:     global_buffer
      - .actual_access:  write_only
        .address_space:  global
        .offset:         16
        .size:           8
        .value_kind:     global_buffer
    .group_segment_fixed_size: 0
    .kernarg_segment_align: 8
    .kernarg_segment_size: 24
    .language:       OpenCL C
    .language_version:
      - 2
      - 0
    .max_flat_workgroup_size: 512
    .name:           _Z9gemm_out2PKtS0_Pf
    .private_segment_fixed_size: 0
    .sgpr_count:     27
    .sgpr_spill_count: 0
    .symbol:         _Z9gemm_out2PKtS0_Pf.kd
    .uniform_work_group_size: 1
    .uses_dynamic_stack: false
    .vgpr_count:     146
    .vgpr_spill_count: 0
    .wavefront_size: 64
  - .agpr_count:     0
    .args:
      - .actual_access:  read_only
        .address_space:  global
        .offset:         0
        .size:           8
        .value_kind:     global_buffer
      - .actual_access:  write_only
        .address_space:  global
        .offset:         8
        .size:           8
        .value_kind:     global_buffer
    .group_segment_fixed_size: 0
    .kernarg_segment_align: 8
    .kernarg_segment_size: 16
    .language:       OpenCL C
    .language_version:
      - 2
      - 0
    .max_flat_workgroup_size: 256
    .name:           _Z6conv_xPKfPt
    .private_segment_fixed_size: 0
    .sgpr_count:     14
    .sgpr_spill_count: 0
    .symbol:         _Z6conv_xPKfPt.kd
    .uniform_work_group_size: 1
    .uses_dynamic_stack: false
    .vgpr_count:     12
    .vgpr_spill_count: 0
    .wavefront_size: 64
  - .agpr_count:     0
    .args:
      - .actual_access:  read_only
        .address_space:  global
        .offset:         0
        .size:           8
        .value_kind:     global_buffer
      - .actual_access:  read_only
        .address_space:  global
        .offset:         8
        .size:           8
        .value_kind:     global_buffer
      - .actual_access:  read_only
        .address_space:  global
        .offset:         16
        .size:           8
        .value_kind:     global_buffer
      - .actual_access:  read_only
        .address_space:  global
        .offset:         24
        .size:           8
        .value_kind:     global_buffer
      - .actual_access:  read_only
        .address_space:  global
        .offset:         32
        .size:           8
        .value_kind:     global_buffer
      - .actual_access:  write_only
        .address_space:  global
        .offset:         40
        .size:           8
        .value_kind:     global_buffer
      - .actual_access:  write_only
        .address_space:  global
        .offset:         48
        .size:           8
        .value_kind:     global_buffer
    .group_segment_fixed_size: 16640
    .kernarg_segment_align: 8
    .kernarg_segment_size: 56
    .language:       OpenCL C
    .language_version:
      - 2
      - 0
    .max_flat_workgroup_size: 256
    .name:           _Z7conv_wTPKfS0_S0_S0_S0_PtS1_
    .private_segment_fixed_size: 0
    .sgpr_count:     26
    .sgpr_spill_count: 0
    .symbol:         _Z7conv_wTPKfS0_S0_S0_S0_PtS1_.kd
    .uniform_work_group_size: 1
    .uses_dynamic_stack: false
    .vgpr_count:     51
    .vgpr_spill_count: 0
    .wavefront_size: 64
  - .agpr_count:     0
    .args:
      - .actual_access:  read_only
        .address_space:  global
        .offset:         0
        .size:           8
        .value_kind:     global_buffer
      - .actual_access:  read_only
        .address_space:  global
        .offset:         8
        .size:           8
        .value_kind:     global_buffer
      - .actual_access:  write_only
        .address_space:  global
        .offset:         16
        .size:           8
        .value_kind:     global_buffer
    .group_segment_fixed_size: 0
    .kernarg_segment_align: 8
    .kernarg_segment_size: 24
    .language:       OpenCL C
    .language_version:
      - 2
      - 0
    .max_flat_workgroup_size: 256
    .name:           _Z7conv_w1PKfS0_Pt
    .private_segment_fixed_size: 0
    .sgpr_count:     16
    .sgpr_spill_count: 0
    .symbol:         _Z7conv_w1PKfS0_Pt.kd
    .uniform_work_group_size: 1
    .uses_dynamic_stack: false
    .vgpr_count:     6
    .vgpr_spill_count: 0
    .wavefront_size: 64
  - .agpr_count:     8
    .args:
      - .actual_access:  read_only
        .address_space:  global
        .offset:         0
        .size:           8
        .value_kind:     global_buffer
      - .actual_access:  read_only
        .address_space:  global
        .offset:         8
        .size:           8
        .value_kind:     global_buffer
      - .actual_access:  read_only
        .address_space:  global
        .offset:         16
        .size:           8
        .value_kind:     global_buffer
      - .actual_access:  read_only
        .address_space:  global
        .offset:         24
        .size:           8
        .value_kind:     global_buffer
      - .actual_access:  read_only
        .address_space:  global
        .offset:         32
        .size:           8
        .value_kind:     global_buffer
      - .actual_access:  read_only
        .address_space:  global
        .offset:         40
        .size:           8
        .value_kind:     global_buffer
      - .actual_access:  write_only
        .address_space:  global
        .offset:         48
        .size:           8
        .value_kind:     global_buffer
      - .actual_access:  write_only
        .address_space:  global
        .offset:         56
        .size:           8
        .value_kind:     global_buffer
      - .actual_access:  write_only
        .address_space:  global
        .offset:         64
        .size:           8
        .value_kind:     global_buffer
    .group_segment_fixed_size: 10240
    .kernarg_segment_align: 8
    .kernarg_segment_size: 72
    .language:       OpenCL C
    .language_version:
      - 2
      - 0
    .max_flat_workgroup_size: 256
    .name:           _Z10gates_fastPKtS0_PKfS2_S2_S2_PtS3_S3_
    .private_segment_fixed_size: 0
    .sgpr_count:     24
    .sgpr_spill_count: 0
    .symbol:         _Z10gates_fastPKtS0_PKfS2_S2_S2_PtS3_S3_.kd
    .uniform_work_group_size: 1
    .uses_dynamic_stack: false
    .vgpr_count:     96
    .vgpr_spill_count: 0
    .wavefront_size: 64
  - .agpr_count:     4
    .args:
      - .actual_access:  read_only
        .address_space:  global
        .offset:         0
        .size:           8
        .value_kind:     global_buffer
      - .actual_access:  read_only
        .address_space:  global
        .offset:         8
        .size:           8
        .value_kind:     global_buffer
      - .actual_access:  read_only
        .address_space:  global
        .offset:         16
        .size:           8
        .value_kind:     global_buffer
      - .actual_access:  read_only
        .address_space:  global
        .offset:         24
        .size:           8
        .value_kind:     global_buffer
      - .actual_access:  write_only
        .address_space:  global
        .offset:         32
        .size:           8
        .value_kind:     global_buffer
      - .actual_access:  write_only
        .address_space:  global
        .offset:         40
        .size:           8
        .value_kind:     global_buffer
      - .actual_access:  write_only
        .address_space:  global
        .offset:         48
        .size:           8
        .value_kind:     global_buffer
    .group_segment_fixed_size: 0
    .kernarg_segment_align: 8
    .kernarg_segment_size: 56
    .language:       OpenCL C
    .language_version:
      - 2
      - 0
    .max_flat_workgroup_size: 256
    .name:           _Z10state_fastPKtS0_S0_S0_PtS1_Pf
    .private_segment_fixed_size: 0
    .sgpr_count:     20
    .sgpr_spill_count: 0
    .symbol:         _Z10state_fastPKtS0_S0_S0_PtS1_Pf.kd
    .uniform_work_group_size: 1
    .uses_dynamic_stack: false
    .vgpr_count:     184
    .vgpr_spill_count: 0
    .wavefront_size: 64
  - .agpr_count:     0
    .args:
      - .actual_access:  read_only
        .address_space:  global
        .offset:         0
        .size:           8
        .value_kind:     global_buffer
      - .actual_access:  read_only
        .address_space:  global
        .offset:         8
        .size:           8
        .value_kind:     global_buffer
      - .actual_access:  read_only
        .address_space:  global
        .offset:         16
        .size:           8
        .value_kind:     global_buffer
      - .actual_access:  write_only
        .address_space:  global
        .offset:         24
        .size:           8
        .value_kind:     global_buffer
      - .actual_access:  write_only
        .address_space:  global
        .offset:         32
        .size:           8
        .value_kind:     global_buffer
      - .actual_access:  write_only
        .address_space:  global
        .offset:         40
        .size:           8
        .value_kind:     global_buffer
    .group_segment_fixed_size: 0
    .kernarg_segment_align: 8
    .kernarg_segment_size: 48
    .language:       OpenCL C
    .language_version:
      - 2
      - 0
    .max_flat_workgroup_size: 256
    .name:           _Z11prefix_fastPKtS0_PKfPtS3_Pf
    .private_segment_fixed_size: 0
    .sgpr_count:     106
    .sgpr_spill_count: 41
    .symbol:         _Z11prefix_fastPKtS0_PKfPtS3_Pf.kd
    .uniform_work_group_size: 1
    .uses_dynamic_stack: false
    .vgpr_count:     205
    .vgpr_spill_count: 0
    .wavefront_size: 64
  - .agpr_count:     0
    .args:
      - .address_space:  global
        .offset:         0
        .size:           8
        .value_kind:     global_buffer
      - .address_space:  global
        .offset:         8
        .size:           8
        .value_kind:     global_buffer
      - .address_space:  global
        .offset:         16
        .size:           8
        .value_kind:     global_buffer
      - .actual_access:  read_only
        .address_space:  global
        .offset:         24
        .size:           8
        .value_kind:     global_buffer
      - .address_space:  global
        .offset:         32
        .size:           8
        .value_kind:     global_buffer
      - .address_space:  global
        .offset:         40
        .size:           8
        .value_kind:     global_buffer
      - .address_space:  global
        .offset:         48
        .size:           8
        .value_kind:     global_buffer
      - .address_space:  global
        .offset:         56
        .size:           8
        .value_kind:     global_buffer
      - .address_space:  global
        .offset:         64
        .size:           8
        .value_kind:     global_buffer
      - .address_space:  global
        .offset:         72
        .size:           8
        .value_kind:     global_buffer
      - .address_space:  global
        .offset:         80
        .size:           8
        .value_kind:     global_buffer
      - .actual_access:  write_only
        .address_space:  global
        .offset:         88
        .size:           8
        .value_kind:     global_buffer
    .group_segment_fixed_size: 0
    .kernarg_segment_align: 8
    .kernarg_segment_size: 96
    .language:       OpenCL C
    .language_version:
      - 2
      - 0
    .max_flat_workgroup_size: 512
    .name:           _Z9attn_fastPKtS0_S0_S0_S0_S0_S0_S0_S0_PKfS2_Pt
    .private_segment_fixed_size: 0
    .sgpr_count:     52
    .sgpr_spill_count: 0
    .symbol:         _Z9attn_fastPKtS0_S0_S0_S0_S0_S0_S0_S0_PKfS2_Pt.kd
    .uniform_work_group_size: 1
    .uses_dynamic_stack: false
    .vgpr_count:     156
    .vgpr_spill_count: 0
    .wavefront_size: 64
  - .agpr_count:     12
    .args:
      - .actual_access:  read_only
        .address_space:  global
        .offset:         0
        .size:           8
        .value_kind:     global_buffer
      - .actual_access:  read_only
        .address_space:  global
        .offset:         8
        .size:           8
        .value_kind:     global_buffer
      - .actual_access:  read_only
        .address_space:  global
        .offset:         16
        .size:           8
        .value_kind:     global_buffer
      - .actual_access:  read_only
        .address_space:  global
        .offset:         24
        .size:           8
        .value_kind:     global_buffer
      - .actual_access:  read_only
        .address_space:  global
        .offset:         32
        .size:           8
        .value_kind:     global_buffer
      - .actual_access:  read_only
        .address_space:  global
        .offset:         40
        .size:           8
        .value_kind:     global_buffer
      - .actual_access:  read_only
        .address_space:  global
        .offset:         48
        .size:           8
        .value_kind:     global_buffer
      - .actual_access:  read_only
        .address_space:  global
        .offset:         56
        .size:           8
        .value_kind:     global_buffer
      - .actual_access:  read_only
        .address_space:  global
        .offset:         64
        .size:           8
        .value_kind:     global_buffer
      - .actual_access:  read_only
        .address_space:  global
        .offset:         72
        .size:           8
        .value_kind:     global_buffer
      - .actual_access:  read_only
        .address_space:  global
        .offset:         80
        .size:           8
        .value_kind:     global_buffer
      - .actual_access:  read_only
        .address_space:  global
        .offset:         88
        .size:           8
        .value_kind:     global_buffer
      - .actual_access:  write_only
        .address_space:  global
        .offset:         96
        .size:           8
        .value_kind:     global_buffer
      - .actual_access:  write_only
        .address_space:  global
        .offset:         104
        .size:           8
        .value_kind:     global_buffer
      - .actual_access:  write_only
        .address_space:  global
        .offset:         112
        .size:           8
        .value_kind:     global_buffer
      - .actual_access:  write_only
        .address_space:  global
        .offset:         120
        .size:           8
        .value_kind:     global_buffer
      - .actual_access:  write_only
        .address_space:  global
        .offset:         128
        .size:           8
        .value_kind:     global_buffer
      - .actual_access:  write_only
        .address_space:  global
        .offset:         136
        .size:           8
        .value_kind:     global_buffer
    .group_segment_fixed_size: 16640
    .kernarg_segment_align: 8
    .kernarg_segment_size: 144
    .language:       OpenCL C
    .language_version:
      - 2
      - 0
    .max_flat_workgroup_size: 256
    .name:           _Z11prep_kernelPKfS0_S0_S0_S0_S0_S0_S0_S0_S0_S0_S0_PtS1_S1_S1_S1_S1_
    .private_segment_fixed_size: 0
    .sgpr_count:     34
    .sgpr_spill_count: 0
    .symbol:         _Z11prep_kernelPKfS0_S0_S0_S0_S0_S0_S0_S0_S0_S0_S0_PtS1_S1_S1_S1_S1_.kd
    .uniform_work_group_size: 1
    .uses_dynamic_stack: false
    .vgpr_count:     124
    .vgpr_spill_count: 0
    .wavefront_size: 64
  - .agpr_count:     0
    .args:
      - .address_space:  global
        .offset:         0
        .size:           8
        .value_kind:     global_buffer
      - .address_space:  global
        .offset:         8
        .size:           8
        .value_kind:     global_buffer
      - .offset:         16
        .size:           4
        .value_kind:     by_value
      - .offset:         20
        .size:           4
        .value_kind:     by_value
      - .offset:         24
        .size:           4
        .value_kind:     by_value
      - .offset:         28
        .size:           4
        .value_kind:     by_value
      - .address_space:  global
        .offset:         32
        .size:           8
        .value_kind:     global_buffer
    .group_segment_fixed_size: 0
    .kernarg_segment_align: 8
    .kernarg_segment_size: 40
    .language:       OpenCL C
    .language_version:
      - 2
      - 0
    .max_flat_workgroup_size: 1024
    .name:           _Z9dbg_cmp16PKtS0_iiffPf
    .private_segment_fixed_size: 0
    .sgpr_count:     18
    .sgpr_spill_count: 0
    .symbol:         _Z9dbg_cmp16PKtS0_iiffPf.kd
    .uniform_work_group_size: 1
    .uses_dynamic_stack: false
    .vgpr_count:     5
    .vgpr_spill_count: 0
    .wavefront_size: 64
  - .agpr_count:     0
    .args:
      - .address_space:  global
        .offset:         0
        .size:           8
        .value_kind:     global_buffer
      - .address_space:  global
        .offset:         8
        .size:           8
        .value_kind:     global_buffer
      - .offset:         16
        .size:           4
        .value_kind:     by_value
      - .offset:         20
        .size:           4
        .value_kind:     by_value
      - .offset:         24
        .size:           56
        .value_kind:     by_value
    .group_segment_fixed_size: 0
    .kernarg_segment_align: 8
    .kernarg_segment_size: 80
    .language:       OpenCL C
    .language_version:
      - 2
      - 0
    .max_flat_workgroup_size: 512
    .name:           _Z5gemm8ILi0EEvPKtS1_ii7EpiArgs
    .private_segment_fixed_size: 0
    .sgpr_count:     36
    .sgpr_spill_count: 0
    .symbol:         _Z5gemm8ILi0EEvPKtS1_ii7EpiArgs.kd
    .uniform_work_group_size: 1
    .uses_dynamic_stack: false
    .vgpr_count:     246
    .vgpr_spill_count: 0
    .wavefront_size: 64
  - .agpr_count:     0
    .args:
      - .address_space:  global
        .offset:         0
        .size:           8
        .value_kind:     global_buffer
      - .address_space:  global
        .offset:         8
        .size:           8
        .value_kind:     global_buffer
      - .address_space:  global
        .offset:         16
        .size:           8
        .value_kind:     global_buffer
      - .address_space:  global
        .offset:         24
        .size:           8
        .value_kind:     global_buffer
      - .actual_access:  write_only
        .address_space:  global
        .offset:         32
        .size:           8
        .value_kind:     global_buffer
      - .actual_access:  write_only
        .address_space:  global
        .offset:         40
        .size:           8
        .value_kind:     global_buffer
      - .actual_access:  write_only
        .address_space:  global
        .offset:         48
        .size:           8
        .value_kind:     global_buffer
    .group_segment_fixed_size: 81920
    .kernarg_segment_align: 8
    .kernarg_segment_size: 56
    .language:       OpenCL C
    .language_version:
      - 2
      - 0
    .max_flat_workgroup_size: 256
    .name:           _Z9scan_fastILb1EEvPKtS1_S1_S1_PtS2_Pf
    .private_segment_fixed_size: 0
    .sgpr_count:     62
    .sgpr_spill_count: 0
    .symbol:         _Z9scan_fastILb1EEvPKtS1_S1_S1_PtS2_Pf.kd
    .uniform_work_group_size: 1
    .uses_dynamic_stack: false
    .vgpr_count:     160
    .vgpr_spill_count: 0
    .wavefront_size: 64
